# v52 with the hand-written compute and loader streams shifted by 4 bytes (code placement check)
# speedup vs baseline: 1.0345x; 1.0299x over previous
.LBB1_235:
	s_nop 0
	v_mov_b32_e32 v110, v18
	v_mov_b32_e32 v111, v19
	v_mov_b32_e32 v112, v20
	v_mov_b32_e32 v113, v21
	s_mov_b32 s72, 0x2000
	s_mov_b32 s73, 0
	s_mov_b32 s74, 0x20000
	s_mov_b32 s75, 0
	v_lshl_add_u64 v[158:159], v[158:159], 0, s[74:75]
	v_mul_u32_u24_e32 v163, 0x110, v160
	v_lshl_add_u32 v162, v1, 4, v163
	global_load_dwordx4 v[94:97], v[158:159], off
	v_lshl_add_u64 v[158:159], v[158:159], 0, s[72:73]
	global_load_dwordx4 v[98:101], v[158:159], off
	v_lshl_add_u64 v[158:159], v[158:159], 0, s[72:73]
	global_load_dwordx4 v[102:105], v[158:159], off
	v_lshl_add_u64 v[158:159], v[158:159], 0, s[72:73]
	global_load_dwordx4 v[106:109], v[158:159], off
	v_lshl_add_u64 v[158:159], v[158:159], 0, s[72:73]
	global_load_dwordx4 v[142:145], v[158:159], off
	v_lshl_add_u64 v[158:159], v[158:159], 0, s[72:73]
	global_load_dwordx4 v[146:149], v[158:159], off
	v_lshl_add_u64 v[158:159], v[158:159], 0, s[72:73]
	global_load_dwordx4 v[150:153], v[158:159], off
	v_lshl_add_u64 v[158:159], v[158:159], 0, s[72:73]
	global_load_dwordx4 v[154:157], v[158:159], off
	v_lshl_add_u64 v[158:159], v[158:159], 0, s[72:73]
	s_waitcnt lgkmcnt(0)
	s_barrier
	ds_read_b128 v[114:117], v162 offset:0
	ds_read_b128 v[118:121], v162 offset:8704
	ds_read_b128 v[122:125], v162 offset:32
	ds_read_b128 v[126:129], v162 offset:8736
	ds_read_b128 v[130:133], v162 offset:64
	ds_read_b128 v[134:137], v162 offset:8768
	s_waitcnt lgkmcnt(5)
	v_mfma_f32_32x32x16_f16 v[2:17], v[114:117], v[110:113], 0
	s_waitcnt lgkmcnt(4)
	v_mfma_f32_32x32x16_f16 v[18:33], v[118:121], v[110:113], 0
	ds_read_b128 v[114:117], v162 offset:96
	ds_read_b128 v[118:121], v162 offset:8800
	global_load_dwordx4 v[110:113], v[158:159], off
	v_lshl_add_u64 v[158:159], v[158:159], 0, s[72:73]
	s_waitcnt lgkmcnt(5)
	v_mfma_f32_32x32x16_f16 v[2:17], v[122:125], v[90:93], v[2:17]
	s_waitcnt lgkmcnt(4)
	v_mfma_f32_32x32x16_f16 v[18:33], v[126:129], v[90:93], v[18:33]
	ds_read_b128 v[122:125], v162 offset:128
	ds_read_b128 v[126:129], v162 offset:8832
	global_load_dwordx4 v[90:93], v[158:159], off
	v_lshl_add_u64 v[158:159], v[158:159], 0, s[72:73]
	s_waitcnt lgkmcnt(5)
	v_mfma_f32_32x32x16_f16 v[2:17], v[130:133], v[86:89], v[2:17]
	s_waitcnt lgkmcnt(4)
	v_mfma_f32_32x32x16_f16 v[18:33], v[134:137], v[86:89], v[18:33]
	ds_read_b128 v[130:133], v162 offset:160
	ds_read_b128 v[134:137], v162 offset:8864
	global_load_dwordx4 v[86:89], v[158:159], off
	v_lshl_add_u64 v[158:159], v[158:159], 0, s[72:73]
	s_waitcnt lgkmcnt(5)
	v_mfma_f32_32x32x16_f16 v[2:17], v[114:117], v[82:85], v[2:17]
	s_waitcnt lgkmcnt(4)
	v_mfma_f32_32x32x16_f16 v[18:33], v[118:121], v[82:85], v[18:33]
	ds_read_b128 v[114:117], v162 offset:192
	ds_read_b128 v[118:121], v162 offset:8896
	global_load_dwordx4 v[82:85], v[158:159], off
	v_lshl_add_u64 v[158:159], v[158:159], 0, s[72:73]
	s_waitcnt lgkmcnt(5)
	v_mfma_f32_32x32x16_f16 v[2:17], v[122:125], v[78:81], v[2:17]
	s_waitcnt lgkmcnt(4)
	v_mfma_f32_32x32x16_f16 v[18:33], v[126:129], v[78:81], v[18:33]
	ds_read_b128 v[122:125], v162 offset:224
	ds_read_b128 v[126:129], v162 offset:8928
	global_load_dwordx4 v[78:81], v[158:159], off
	v_lshl_add_u64 v[158:159], v[158:159], 0, s[72:73]
	s_waitcnt lgkmcnt(5)
	v_mfma_f32_32x32x16_f16 v[2:17], v[130:133], v[74:77], v[2:17]
	s_waitcnt lgkmcnt(4)
	v_mfma_f32_32x32x16_f16 v[18:33], v[134:137], v[74:77], v[18:33]
	global_load_dwordx4 v[74:77], v[158:159], off
	v_lshl_add_u64 v[158:159], v[158:159], 0, s[72:73]
	s_waitcnt lgkmcnt(3)
	v_mfma_f32_32x32x16_f16 v[2:17], v[114:117], v[70:73], v[2:17]
	s_waitcnt lgkmcnt(2)
	v_mfma_f32_32x32x16_f16 v[18:33], v[118:121], v[70:73], v[18:33]
	global_load_dwordx4 v[70:73], v[158:159], off
	v_lshl_add_u64 v[158:159], v[158:159], 0, s[72:73]
	s_waitcnt lgkmcnt(1)
	v_mfma_f32_32x32x16_f16 v[2:17], v[122:125], v[66:69], v[2:17]
	s_waitcnt lgkmcnt(0)
	v_mfma_f32_32x32x16_f16 v[18:33], v[126:129], v[66:69], v[18:33]
	global_load_dwordx4 v[66:69], v[158:159], off
	v_lshl_add_u64 v[158:159], v[158:159], 0, s[72:73]
	s_waitcnt lgkmcnt(0)
	s_barrier
	ds_read_b128 v[114:117], v162 offset:17408
	ds_read_b128 v[118:121], v162 offset:26112
	ds_read_b128 v[122:125], v162 offset:17440
	ds_read_b128 v[126:129], v162 offset:26144
	ds_read_b128 v[130:133], v162 offset:17472
	ds_read_b128 v[134:137], v162 offset:26176
	s_waitcnt lgkmcnt(5)
	v_mfma_f32_32x32x16_f16 v[2:17], v[114:117], v[62:65], v[2:17]
	s_waitcnt lgkmcnt(4)
	v_mfma_f32_32x32x16_f16 v[18:33], v[118:121], v[62:65], v[18:33]
	ds_read_b128 v[114:117], v162 offset:17504
	ds_read_b128 v[118:121], v162 offset:26208
	global_load_dwordx4 v[62:65], v[158:159], off
	v_lshl_add_u64 v[158:159], v[158:159], 0, s[72:73]
	s_waitcnt lgkmcnt(5)
	v_mfma_f32_32x32x16_f16 v[2:17], v[122:125], v[58:61], v[2:17]
	s_waitcnt lgkmcnt(4)
	v_mfma_f32_32x32x16_f16 v[18:33], v[126:129], v[58:61], v[18:33]
	ds_read_b128 v[122:125], v162 offset:17536
	ds_read_b128 v[126:129], v162 offset:26240
	global_load_dwordx4 v[58:61], v[158:159], off
	v_lshl_add_u64 v[158:159], v[158:159], 0, s[72:73]
	s_waitcnt lgkmcnt(5)
	v_mfma_f32_32x32x16_f16 v[2:17], v[130:133], v[54:57], v[2:17]
	s_waitcnt lgkmcnt(4)
	v_mfma_f32_32x32x16_f16 v[18:33], v[134:137], v[54:57], v[18:33]
	ds_read_b128 v[130:133], v162 offset:17568
	ds_read_b128 v[134:137], v162 offset:26272
	global_load_dwordx4 v[54:57], v[158:159], off
	v_lshl_add_u64 v[158:159], v[158:159], 0, s[72:73]
	s_waitcnt lgkmcnt(5)
	v_mfma_f32_32x32x16_f16 v[2:17], v[114:117], v[50:53], v[2:17]
	s_waitcnt lgkmcnt(4)
	v_mfma_f32_32x32x16_f16 v[18:33], v[118:121], v[50:53], v[18:33]
	ds_read_b128 v[114:117], v162 offset:17600
	ds_read_b128 v[118:121], v162 offset:26304
	global_load_dwordx4 v[50:53], v[158:159], off
	v_lshl_add_u64 v[158:159], v[158:159], 0, s[72:73]
	s_waitcnt lgkmcnt(5)
	v_mfma_f32_32x32x16_f16 v[2:17], v[122:125], v[46:49], v[2:17]
	s_waitcnt lgkmcnt(4)
	v_mfma_f32_32x32x16_f16 v[18:33], v[126:129], v[46:49], v[18:33]
	ds_read_b128 v[122:125], v162 offset:17632
	ds_read_b128 v[126:129], v162 offset:26336
	global_load_dwordx4 v[46:49], v[158:159], off
	v_lshl_add_u64 v[158:159], v[158:159], 0, s[72:73]
	s_waitcnt lgkmcnt(5)
	v_mfma_f32_32x32x16_f16 v[2:17], v[130:133], v[42:45], v[2:17]
	s_waitcnt lgkmcnt(4)
	v_mfma_f32_32x32x16_f16 v[18:33], v[134:137], v[42:45], v[18:33]
	global_load_dwordx4 v[42:45], v[158:159], off
	v_lshl_add_u64 v[158:159], v[158:159], 0, s[72:73]
	s_waitcnt lgkmcnt(3)
	v_mfma_f32_32x32x16_f16 v[2:17], v[114:117], v[38:41], v[2:17]
	s_waitcnt lgkmcnt(2)
	v_mfma_f32_32x32x16_f16 v[18:33], v[118:121], v[38:41], v[18:33]
	global_load_dwordx4 v[38:41], v[158:159], off
	v_lshl_add_u64 v[158:159], v[158:159], 0, s[72:73]
	s_waitcnt lgkmcnt(1)
	v_mfma_f32_32x32x16_f16 v[2:17], v[122:125], v[34:37], v[2:17]
	s_waitcnt lgkmcnt(0)
	v_mfma_f32_32x32x16_f16 v[18:33], v[126:129], v[34:37], v[18:33]
	global_load_dwordx4 v[34:37], v[158:159], off
	v_lshl_add_u64 v[158:159], v[158:159], 0, s[72:73]
	s_waitcnt lgkmcnt(0)
	s_barrier
	ds_read_b128 v[114:117], v162 offset:34816
	ds_read_b128 v[118:121], v162 offset:43520
	ds_read_b128 v[122:125], v162 offset:34848
	ds_read_b128 v[126:129], v162 offset:43552
	ds_read_b128 v[130:133], v162 offset:34880
	ds_read_b128 v[134:137], v162 offset:43584
	s_waitcnt vmcnt(23)
	s_waitcnt lgkmcnt(5)
	v_mfma_f32_32x32x16_f16 v[2:17], v[114:117], v[94:97], v[2:17]
	s_waitcnt lgkmcnt(4)
	v_mfma_f32_32x32x16_f16 v[18:33], v[118:121], v[94:97], v[18:33]
	ds_read_b128 v[114:117], v162 offset:34912
	ds_read_b128 v[118:121], v162 offset:43616
	global_load_dwordx4 v[94:97], v[158:159], off
	v_lshl_add_u64 v[158:159], v[158:159], 0, s[72:73]
	s_waitcnt vmcnt(23)
	s_waitcnt lgkmcnt(5)
	v_mfma_f32_32x32x16_f16 v[2:17], v[122:125], v[98:101], v[2:17]
	s_waitcnt lgkmcnt(4)
	v_mfma_f32_32x32x16_f16 v[18:33], v[126:129], v[98:101], v[18:33]
	ds_read_b128 v[122:125], v162 offset:34944
	ds_read_b128 v[126:129], v162 offset:43648
	global_load_dwordx4 v[98:101], v[158:159], off
	v_lshl_add_u64 v[158:159], v[158:159], 0, s[72:73]
	s_waitcnt vmcnt(23)
	s_waitcnt lgkmcnt(5)
	v_mfma_f32_32x32x16_f16 v[2:17], v[130:133], v[102:105], v[2:17]
	s_waitcnt lgkmcnt(4)
	v_mfma_f32_32x32x16_f16 v[18:33], v[134:137], v[102:105], v[18:33]
	ds_read_b128 v[130:133], v162 offset:34976
	ds_read_b128 v[134:137], v162 offset:43680
	global_load_dwordx4 v[102:105], v[158:159], off
	v_lshl_add_u64 v[158:159], v[158:159], 0, s[72:73]
	s_waitcnt vmcnt(23)
	s_waitcnt lgkmcnt(5)
	v_mfma_f32_32x32x16_f16 v[2:17], v[114:117], v[106:109], v[2:17]
	s_waitcnt lgkmcnt(4)
	v_mfma_f32_32x32x16_f16 v[18:33], v[118:121], v[106:109], v[18:33]
	ds_read_b128 v[114:117], v162 offset:35008
	ds_read_b128 v[118:121], v162 offset:43712
	global_load_dwordx4 v[106:109], v[158:159], off
	v_lshl_add_u64 v[158:159], v[158:159], 0, s[72:73]
	s_waitcnt vmcnt(23)
	s_waitcnt lgkmcnt(5)
	v_mfma_f32_32x32x16_f16 v[2:17], v[122:125], v[142:145], v[2:17]
	s_waitcnt lgkmcnt(4)
	v_mfma_f32_32x32x16_f16 v[18:33], v[126:129], v[142:145], v[18:33]
	ds_read_b128 v[122:125], v162 offset:35040
	ds_read_b128 v[126:129], v162 offset:43744
	global_load_dwordx4 v[142:145], v[158:159], off
	v_lshl_add_u64 v[158:159], v[158:159], 0, s[72:73]
	s_waitcnt vmcnt(23)
	s_waitcnt lgkmcnt(5)
	v_mfma_f32_32x32x16_f16 v[2:17], v[130:133], v[146:149], v[2:17]
	s_waitcnt lgkmcnt(4)
	v_mfma_f32_32x32x16_f16 v[18:33], v[134:137], v[146:149], v[18:33]
	global_load_dwordx4 v[146:149], v[158:159], off
	v_lshl_add_u64 v[158:159], v[158:159], 0, s[72:73]
	s_waitcnt vmcnt(23)
	s_waitcnt lgkmcnt(3)
	v_mfma_f32_32x32x16_f16 v[2:17], v[114:117], v[150:153], v[2:17]
	s_waitcnt lgkmcnt(2)
	v_mfma_f32_32x32x16_f16 v[18:33], v[118:121], v[150:153], v[18:33]
	global_load_dwordx4 v[150:153], v[158:159], off
	v_lshl_add_u64 v[158:159], v[158:159], 0, s[72:73]
	s_waitcnt vmcnt(23)
	s_waitcnt lgkmcnt(1)
	v_mfma_f32_32x32x16_f16 v[2:17], v[122:125], v[154:157], v[2:17]
	s_waitcnt lgkmcnt(0)
	v_mfma_f32_32x32x16_f16 v[18:33], v[126:129], v[154:157], v[18:33]
	global_load_dwordx4 v[154:157], v[158:159], off
	v_lshl_add_u64 v[158:159], v[158:159], 0, s[72:73]
	s_waitcnt lgkmcnt(0)
	s_barrier
	ds_read_b128 v[114:117], v162 offset:52224
	ds_read_b128 v[118:121], v162 offset:60928
	ds_read_b128 v[122:125], v162 offset:52256
	ds_read_b128 v[126:129], v162 offset:60960
	ds_read_b128 v[130:133], v162 offset:52288
	ds_read_b128 v[134:137], v162 offset:60992
	s_waitcnt vmcnt(23)
	s_waitcnt lgkmcnt(5)
	v_mfma_f32_32x32x16_f16 v[2:17], v[114:117], v[110:113], v[2:17]
	s_waitcnt lgkmcnt(4)
	v_mfma_f32_32x32x16_f16 v[18:33], v[118:121], v[110:113], v[18:33]
	ds_read_b128 v[114:117], v162 offset:52320
	ds_read_b128 v[118:121], v162 offset:61024
	global_load_dwordx4 v[110:113], v[158:159], off
	v_lshl_add_u64 v[158:159], v[158:159], 0, s[72:73]
	s_waitcnt vmcnt(23)
	s_waitcnt lgkmcnt(5)
	v_mfma_f32_32x32x16_f16 v[2:17], v[122:125], v[90:93], v[2:17]
	s_waitcnt lgkmcnt(4)
	v_mfma_f32_32x32x16_f16 v[18:33], v[126:129], v[90:93], v[18:33]
	ds_read_b128 v[122:125], v162 offset:52352
	ds_read_b128 v[126:129], v162 offset:61056
	global_load_dwordx4 v[90:93], v[158:159], off
	v_lshl_add_u64 v[158:159], v[158:159], 0, s[72:73]
	s_waitcnt vmcnt(23)
	s_waitcnt lgkmcnt(5)
	v_mfma_f32_32x32x16_f16 v[2:17], v[130:133], v[86:89], v[2:17]
	s_waitcnt lgkmcnt(4)
	v_mfma_f32_32x32x16_f16 v[18:33], v[134:137], v[86:89], v[18:33]
	ds_read_b128 v[130:133], v162 offset:52384
	ds_read_b128 v[134:137], v162 offset:61088
	global_load_dwordx4 v[86:89], v[158:159], off
	v_lshl_add_u64 v[158:159], v[158:159], 0, s[72:73]
	s_waitcnt vmcnt(23)
	s_waitcnt lgkmcnt(5)
	v_mfma_f32_32x32x16_f16 v[2:17], v[114:117], v[82:85], v[2:17]
	s_waitcnt lgkmcnt(4)
	v_mfma_f32_32x32x16_f16 v[18:33], v[118:121], v[82:85], v[18:33]
	ds_read_b128 v[114:117], v162 offset:52416
	ds_read_b128 v[118:121], v162 offset:61120
	global_load_dwordx4 v[82:85], v[158:159], off
	v_lshl_add_u64 v[158:159], v[158:159], 0, s[72:73]
	s_waitcnt vmcnt(23)
	s_waitcnt lgkmcnt(5)
	v_mfma_f32_32x32x16_f16 v[2:17], v[122:125], v[78:81], v[2:17]
	s_waitcnt lgkmcnt(4)
	v_mfma_f32_32x32x16_f16 v[18:33], v[126:129], v[78:81], v[18:33]
	ds_read_b128 v[122:125], v162 offset:52448
	ds_read_b128 v[126:129], v162 offset:61152
	global_load_dwordx4 v[78:81], v[158:159], off
	v_lshl_add_u64 v[158:159], v[158:159], 0, s[72:73]
	s_waitcnt vmcnt(23)
	s_waitcnt lgkmcnt(5)
	v_mfma_f32_32x32x16_f16 v[2:17], v[130:133], v[74:77], v[2:17]
	s_waitcnt lgkmcnt(4)
	v_mfma_f32_32x32x16_f16 v[18:33], v[134:137], v[74:77], v[18:33]
	global_load_dwordx4 v[74:77], v[158:159], off
	v_lshl_add_u64 v[158:159], v[158:159], 0, s[72:73]
	s_waitcnt vmcnt(23)
	s_waitcnt lgkmcnt(3)
	v_mfma_f32_32x32x16_f16 v[2:17], v[114:117], v[70:73], v[2:17]
	s_waitcnt lgkmcnt(2)
	v_mfma_f32_32x32x16_f16 v[18:33], v[118:121], v[70:73], v[18:33]
	global_load_dwordx4 v[70:73], v[158:159], off
	v_lshl_add_u64 v[158:159], v[158:159], 0, s[72:73]
	s_waitcnt vmcnt(23)
	s_waitcnt lgkmcnt(1)
	v_mfma_f32_32x32x16_f16 v[2:17], v[122:125], v[66:69], v[2:17]
	s_waitcnt lgkmcnt(0)
	v_mfma_f32_32x32x16_f16 v[18:33], v[126:129], v[66:69], v[18:33]
	global_load_dwordx4 v[66:69], v[158:159], off
	v_lshl_add_u64 v[158:159], v[158:159], 0, s[72:73]
	s_waitcnt lgkmcnt(0)
	s_barrier
	ds_read_b128 v[114:117], v162 offset:0
	ds_read_b128 v[118:121], v162 offset:8704
	ds_read_b128 v[122:125], v162 offset:32
	ds_read_b128 v[126:129], v162 offset:8736
	ds_read_b128 v[130:133], v162 offset:64
	ds_read_b128 v[134:137], v162 offset:8768
	s_waitcnt vmcnt(23)
	s_waitcnt lgkmcnt(5)
	v_mfma_f32_32x32x16_f16 v[2:17], v[114:117], v[62:65], v[2:17]
	s_waitcnt lgkmcnt(4)
	v_mfma_f32_32x32x16_f16 v[18:33], v[118:121], v[62:65], v[18:33]
	ds_read_b128 v[114:117], v162 offset:96
	ds_read_b128 v[118:121], v162 offset:8800
	global_load_dwordx4 v[62:65], v[158:159], off
	v_lshl_add_u64 v[158:159], v[158:159], 0, s[72:73]
	s_waitcnt vmcnt(23)
	s_waitcnt lgkmcnt(5)
	v_mfma_f32_32x32x16_f16 v[2:17], v[122:125], v[58:61], v[2:17]
	s_waitcnt lgkmcnt(4)
	v_mfma_f32_32x32x16_f16 v[18:33], v[126:129], v[58:61], v[18:33]
	ds_read_b128 v[122:125], v162 offset:128
	ds_read_b128 v[126:129], v162 offset:8832
	global_load_dwordx4 v[58:61], v[158:159], off
	v_lshl_add_u64 v[158:159], v[158:159], 0, s[72:73]
	s_waitcnt vmcnt(23)
	s_waitcnt lgkmcnt(5)
	v_mfma_f32_32x32x16_f16 v[2:17], v[130:133], v[54:57], v[2:17]
	s_waitcnt lgkmcnt(4)
	v_mfma_f32_32x32x16_f16 v[18:33], v[134:137], v[54:57], v[18:33]
	ds_read_b128 v[130:133], v162 offset:160
	ds_read_b128 v[134:137], v162 offset:8864
	global_load_dwordx4 v[54:57], v[158:159], off
	v_lshl_add_u64 v[158:159], v[158:159], 0, s[72:73]
	s_waitcnt vmcnt(23)
	s_waitcnt lgkmcnt(5)
	v_mfma_f32_32x32x16_f16 v[2:17], v[114:117], v[50:53], v[2:17]
	s_waitcnt lgkmcnt(4)
	v_mfma_f32_32x32x16_f16 v[18:33], v[118:121], v[50:53], v[18:33]
	ds_read_b128 v[114:117], v162 offset:192
	ds_read_b128 v[118:121], v162 offset:8896
	global_load_dwordx4 v[50:53], v[158:159], off
	v_lshl_add_u64 v[158:159], v[158:159], 0, s[72:73]
	s_waitcnt vmcnt(23)
	s_waitcnt lgkmcnt(5)
	v_mfma_f32_32x32x16_f16 v[2:17], v[122:125], v[46:49], v[2:17]
	s_waitcnt lgkmcnt(4)
	v_mfma_f32_32x32x16_f16 v[18:33], v[126:129], v[46:49], v[18:33]
	ds_read_b128 v[122:125], v162 offset:224
	ds_read_b128 v[126:129], v162 offset:8928
	global_load_dwordx4 v[46:49], v[158:159], off
	v_lshl_add_u64 v[158:159], v[158:159], 0, s[72:73]
	s_waitcnt vmcnt(23)
	s_waitcnt lgkmcnt(5)
	v_mfma_f32_32x32x16_f16 v[2:17], v[130:133], v[42:45], v[2:17]
	s_waitcnt lgkmcnt(4)
	v_mfma_f32_32x32x16_f16 v[18:33], v[134:137], v[42:45], v[18:33]
	global_load_dwordx4 v[42:45], v[158:159], off
	v_lshl_add_u64 v[158:159], v[158:159], 0, s[72:73]
	s_waitcnt vmcnt(23)
	s_waitcnt lgkmcnt(3)
	v_mfma_f32_32x32x16_f16 v[2:17], v[114:117], v[38:41], v[2:17]
	s_waitcnt lgkmcnt(2)
	v_mfma_f32_32x32x16_f16 v[18:33], v[118:121], v[38:41], v[18:33]
	global_load_dwordx4 v[38:41], v[158:159], off
	v_lshl_add_u64 v[158:159], v[158:159], 0, s[72:73]
	s_waitcnt vmcnt(23)
	s_waitcnt lgkmcnt(1)
	v_mfma_f32_32x32x16_f16 v[2:17], v[122:125], v[34:37], v[2:17]
	s_waitcnt lgkmcnt(0)
	v_mfma_f32_32x32x16_f16 v[18:33], v[126:129], v[34:37], v[18:33]
	global_load_dwordx4 v[34:37], v[158:159], off
	v_lshl_add_u64 v[158:159], v[158:159], 0, s[72:73]
	s_waitcnt lgkmcnt(0)
	s_barrier
	ds_read_b128 v[114:117], v162 offset:17408
	ds_read_b128 v[118:121], v162 offset:26112
	ds_read_b128 v[122:125], v162 offset:17440
	ds_read_b128 v[126:129], v162 offset:26144
	ds_read_b128 v[130:133], v162 offset:17472
	ds_read_b128 v[134:137], v162 offset:26176
	s_waitcnt vmcnt(23)
	s_waitcnt lgkmcnt(5)
	v_mfma_f32_32x32x16_f16 v[2:17], v[114:117], v[94:97], v[2:17]
	s_waitcnt lgkmcnt(4)
	v_mfma_f32_32x32x16_f16 v[18:33], v[118:121], v[94:97], v[18:33]
	ds_read_b128 v[114:117], v162 offset:17504
	ds_read_b128 v[118:121], v162 offset:26208
	global_load_dwordx4 v[94:97], v[158:159], off
	v_lshl_add_u64 v[158:159], v[158:159], 0, s[72:73]
	s_waitcnt vmcnt(23)
	s_waitcnt lgkmcnt(5)
	v_mfma_f32_32x32x16_f16 v[2:17], v[122:125], v[98:101], v[2:17]
	s_waitcnt lgkmcnt(4)
	v_mfma_f32_32x32x16_f16 v[18:33], v[126:129], v[98:101], v[18:33]
	ds_read_b128 v[122:125], v162 offset:17536
	ds_read_b128 v[126:129], v162 offset:26240
	global_load_dwordx4 v[98:101], v[158:159], off
	v_lshl_add_u64 v[158:159], v[158:159], 0, s[72:73]
	s_waitcnt vmcnt(23)
	s_waitcnt lgkmcnt(5)
	v_mfma_f32_32x32x16_f16 v[2:17], v[130:133], v[102:105], v[2:17]
	s_waitcnt lgkmcnt(4)
	v_mfma_f32_32x32x16_f16 v[18:33], v[134:137], v[102:105], v[18:33]
	ds_read_b128 v[130:133], v162 offset:17568
	ds_read_b128 v[134:137], v162 offset:26272
	global_load_dwordx4 v[102:105], v[158:159], off
	v_lshl_add_u64 v[158:159], v[158:159], 0, s[72:73]
	s_waitcnt vmcnt(23)
	s_waitcnt lgkmcnt(5)
	v_mfma_f32_32x32x16_f16 v[2:17], v[114:117], v[106:109], v[2:17]
	s_waitcnt lgkmcnt(4)
	v_mfma_f32_32x32x16_f16 v[18:33], v[118:121], v[106:109], v[18:33]
	ds_read_b128 v[114:117], v162 offset:17600
	ds_read_b128 v[118:121], v162 offset:26304
	global_load_dwordx4 v[106:109], v[158:159], off
	v_lshl_add_u64 v[158:159], v[158:159], 0, s[72:73]
	s_waitcnt vmcnt(23)
	s_waitcnt lgkmcnt(5)
	v_mfma_f32_32x32x16_f16 v[2:17], v[122:125], v[142:145], v[2:17]
	s_waitcnt lgkmcnt(4)
	v_mfma_f32_32x32x16_f16 v[18:33], v[126:129], v[142:145], v[18:33]
	ds_read_b128 v[122:125], v162 offset:17632
	ds_read_b128 v[126:129], v162 offset:26336
	global_load_dwordx4 v[142:145], v[158:159], off
	v_lshl_add_u64 v[158:159], v[158:159], 0, s[72:73]
	s_waitcnt vmcnt(23)
	s_waitcnt lgkmcnt(5)
	v_mfma_f32_32x32x16_f16 v[2:17], v[130:133], v[146:149], v[2:17]
	s_waitcnt lgkmcnt(4)
	v_mfma_f32_32x32x16_f16 v[18:33], v[134:137], v[146:149], v[18:33]
	global_load_dwordx4 v[146:149], v[158:159], off
	v_lshl_add_u64 v[158:159], v[158:159], 0, s[72:73]
	s_waitcnt vmcnt(23)
	s_waitcnt lgkmcnt(3)
	v_mfma_f32_32x32x16_f16 v[2:17], v[114:117], v[150:153], v[2:17]
	s_waitcnt lgkmcnt(2)
	v_mfma_f32_32x32x16_f16 v[18:33], v[118:121], v[150:153], v[18:33]
	global_load_dwordx4 v[150:153], v[158:159], off
	v_lshl_add_u64 v[158:159], v[158:159], 0, s[72:73]
	s_waitcnt vmcnt(23)
	s_waitcnt lgkmcnt(1)
	v_mfma_f32_32x32x16_f16 v[2:17], v[122:125], v[154:157], v[2:17]
	s_waitcnt lgkmcnt(0)
	v_mfma_f32_32x32x16_f16 v[18:33], v[126:129], v[154:157], v[18:33]
	global_load_dwordx4 v[154:157], v[158:159], off
	v_lshl_add_u64 v[158:159], v[158:159], 0, s[72:73]
	s_waitcnt lgkmcnt(0)
	s_barrier
	ds_read_b128 v[114:117], v162 offset:34816
	ds_read_b128 v[118:121], v162 offset:43520
	ds_read_b128 v[122:125], v162 offset:34848
	ds_read_b128 v[126:129], v162 offset:43552
	ds_read_b128 v[130:133], v162 offset:34880
	ds_read_b128 v[134:137], v162 offset:43584
	s_waitcnt vmcnt(23)
	s_waitcnt lgkmcnt(5)
	v_mfma_f32_32x32x16_f16 v[2:17], v[114:117], v[110:113], v[2:17]
	s_waitcnt lgkmcnt(4)
	v_mfma_f32_32x32x16_f16 v[18:33], v[118:121], v[110:113], v[18:33]
	ds_read_b128 v[114:117], v162 offset:34912
	ds_read_b128 v[118:121], v162 offset:43616
	global_load_dwordx4 v[110:113], v[158:159], off
	v_lshl_add_u64 v[158:159], v[158:159], 0, s[72:73]
	s_waitcnt vmcnt(23)
	s_waitcnt lgkmcnt(5)
	v_mfma_f32_32x32x16_f16 v[2:17], v[122:125], v[90:93], v[2:17]
	s_waitcnt lgkmcnt(4)
	v_mfma_f32_32x32x16_f16 v[18:33], v[126:129], v[90:93], v[18:33]
	ds_read_b128 v[122:125], v162 offset:34944
	ds_read_b128 v[126:129], v162 offset:43648
	global_load_dwordx4 v[90:93], v[158:159], off
	v_lshl_add_u64 v[158:159], v[158:159], 0, s[72:73]
	s_waitcnt vmcnt(23)
	s_waitcnt lgkmcnt(5)
	v_mfma_f32_32x32x16_f16 v[2:17], v[130:133], v[86:89], v[2:17]
	s_waitcnt lgkmcnt(4)
	v_mfma_f32_32x32x16_f16 v[18:33], v[134:137], v[86:89], v[18:33]
	ds_read_b128 v[130:133], v162 offset:34976
	ds_read_b128 v[134:137], v162 offset:43680
	global_load_dwordx4 v[86:89], v[158:159], off
	v_lshl_add_u64 v[158:159], v[158:159], 0, s[72:73]
	s_waitcnt vmcnt(23)
	s_waitcnt lgkmcnt(5)
	v_mfma_f32_32x32x16_f16 v[2:17], v[114:117], v[82:85], v[2:17]
	s_waitcnt lgkmcnt(4)
	v_mfma_f32_32x32x16_f16 v[18:33], v[118:121], v[82:85], v[18:33]
	ds_read_b128 v[114:117], v162 offset:35008
	ds_read_b128 v[118:121], v162 offset:43712
	global_load_dwordx4 v[82:85], v[158:159], off
	v_lshl_add_u64 v[158:159], v[158:159], 0, s[72:73]
	s_waitcnt vmcnt(23)
	s_waitcnt lgkmcnt(5)
	v_mfma_f32_32x32x16_f16 v[2:17], v[122:125], v[78:81], v[2:17]
	s_waitcnt lgkmcnt(4)
	v_mfma_f32_32x32x16_f16 v[18:33], v[126:129], v[78:81], v[18:33]
	ds_read_b128 v[122:125], v162 offset:35040
	ds_read_b128 v[126:129], v162 offset:43744
	global_load_dwordx4 v[78:81], v[158:159], off
	v_lshl_add_u64 v[158:159], v[158:159], 0, s[72:73]
	s_waitcnt vmcnt(23)
	s_waitcnt lgkmcnt(5)
	v_mfma_f32_32x32x16_f16 v[2:17], v[130:133], v[74:77], v[2:17]
	s_waitcnt lgkmcnt(4)
	v_mfma_f32_32x32x16_f16 v[18:33], v[134:137], v[74:77], v[18:33]
	global_load_dwordx4 v[74:77], v[158:159], off
	v_lshl_add_u64 v[158:159], v[158:159], 0, s[72:73]
	s_waitcnt vmcnt(23)
	s_waitcnt lgkmcnt(3)
	v_mfma_f32_32x32x16_f16 v[2:17], v[114:117], v[70:73], v[2:17]
	s_waitcnt lgkmcnt(2)
	v_mfma_f32_32x32x16_f16 v[18:33], v[118:121], v[70:73], v[18:33]
	global_load_dwordx4 v[70:73], v[158:159], off
	v_lshl_add_u64 v[158:159], v[158:159], 0, s[72:73]
	s_waitcnt vmcnt(23)
	s_waitcnt lgkmcnt(1)
	v_mfma_f32_32x32x16_f16 v[2:17], v[122:125], v[66:69], v[2:17]
	s_waitcnt lgkmcnt(0)
	v_mfma_f32_32x32x16_f16 v[18:33], v[126:129], v[66:69], v[18:33]
	global_load_dwordx4 v[66:69], v[158:159], off
	v_lshl_add_u64 v[158:159], v[158:159], 0, s[72:73]
	s_waitcnt lgkmcnt(0)
	s_barrier
	ds_read_b128 v[114:117], v162 offset:52224
	ds_read_b128 v[118:121], v162 offset:60928
	ds_read_b128 v[122:125], v162 offset:52256
	ds_read_b128 v[126:129], v162 offset:60960
	ds_read_b128 v[130:133], v162 offset:52288
	ds_read_b128 v[134:137], v162 offset:60992
	s_waitcnt vmcnt(23)
	s_waitcnt lgkmcnt(5)
	v_mfma_f32_32x32x16_f16 v[2:17], v[114:117], v[62:65], v[2:17]
	s_waitcnt lgkmcnt(4)
	v_mfma_f32_32x32x16_f16 v[18:33], v[118:121], v[62:65], v[18:33]
	ds_read_b128 v[114:117], v162 offset:52320
	ds_read_b128 v[118:121], v162 offset:61024
	global_load_dwordx4 v[62:65], v[158:159], off
	v_lshl_add_u64 v[158:159], v[158:159], 0, s[72:73]
	s_waitcnt vmcnt(23)
	s_waitcnt lgkmcnt(5)
	v_mfma_f32_32x32x16_f16 v[2:17], v[122:125], v[58:61], v[2:17]
	s_waitcnt lgkmcnt(4)
	v_mfma_f32_32x32x16_f16 v[18:33], v[126:129], v[58:61], v[18:33]
	ds_read_b128 v[122:125], v162 offset:52352
	ds_read_b128 v[126:129], v162 offset:61056
	global_load_dwordx4 v[58:61], v[158:159], off
	v_lshl_add_u64 v[158:159], v[158:159], 0, s[72:73]
	s_waitcnt vmcnt(23)
	s_waitcnt lgkmcnt(5)
	v_mfma_f32_32x32x16_f16 v[2:17], v[130:133], v[54:57], v[2:17]
	s_waitcnt lgkmcnt(4)
	v_mfma_f32_32x32x16_f16 v[18:33], v[134:137], v[54:57], v[18:33]
	ds_read_b128 v[130:133], v162 offset:52384
	ds_read_b128 v[134:137], v162 offset:61088
	global_load_dwordx4 v[54:57], v[158:159], off
	v_lshl_add_u64 v[158:159], v[158:159], 0, s[72:73]
	s_waitcnt vmcnt(23)
	s_waitcnt lgkmcnt(5)
	v_mfma_f32_32x32x16_f16 v[2:17], v[114:117], v[50:53], v[2:17]
	s_waitcnt lgkmcnt(4)
	v_mfma_f32_32x32x16_f16 v[18:33], v[118:121], v[50:53], v[18:33]
	ds_read_b128 v[114:117], v162 offset:52416
	ds_read_b128 v[118:121], v162 offset:61120
	global_load_dwordx4 v[50:53], v[158:159], off
	v_lshl_add_u64 v[158:159], v[158:159], 0, s[72:73]
	s_waitcnt vmcnt(23)
	s_waitcnt lgkmcnt(5)
	v_mfma_f32_32x32x16_f16 v[2:17], v[122:125], v[46:49], v[2:17]
	s_waitcnt lgkmcnt(4)
	v_mfma_f32_32x32x16_f16 v[18:33], v[126:129], v[46:49], v[18:33]
	ds_read_b128 v[122:125], v162 offset:52448
	ds_read_b128 v[126:129], v162 offset:61152
	global_load_dwordx4 v[46:49], v[158:159], off
	v_lshl_add_u64 v[158:159], v[158:159], 0, s[72:73]
	s_waitcnt vmcnt(23)
	s_waitcnt lgkmcnt(5)
	v_mfma_f32_32x32x16_f16 v[2:17], v[130:133], v[42:45], v[2:17]
	s_waitcnt lgkmcnt(4)
	v_mfma_f32_32x32x16_f16 v[18:33], v[134:137], v[42:45], v[18:33]
	global_load_dwordx4 v[42:45], v[158:159], off
	v_lshl_add_u64 v[158:159], v[158:159], 0, s[72:73]
	s_waitcnt vmcnt(23)
	s_waitcnt lgkmcnt(3)
	v_mfma_f32_32x32x16_f16 v[2:17], v[114:117], v[38:41], v[2:17]
	s_waitcnt lgkmcnt(2)
	v_mfma_f32_32x32x16_f16 v[18:33], v[118:121], v[38:41], v[18:33]
	global_load_dwordx4 v[38:41], v[158:159], off
	v_lshl_add_u64 v[158:159], v[158:159], 0, s[72:73]
	s_waitcnt vmcnt(23)
	s_waitcnt lgkmcnt(1)
	v_mfma_f32_32x32x16_f16 v[2:17], v[122:125], v[34:37], v[2:17]
	s_waitcnt lgkmcnt(0)
	v_mfma_f32_32x32x16_f16 v[18:33], v[126:129], v[34:37], v[18:33]
	global_load_dwordx4 v[34:37], v[158:159], off
	v_lshl_add_u64 v[158:159], v[158:159], 0, s[72:73]
	s_waitcnt lgkmcnt(0)
	s_barrier
	ds_read_b128 v[114:117], v162 offset:0
	ds_read_b128 v[118:121], v162 offset:8704
	ds_read_b128 v[122:125], v162 offset:32
	ds_read_b128 v[126:129], v162 offset:8736
	ds_read_b128 v[130:133], v162 offset:64
	ds_read_b128 v[134:137], v162 offset:8768
	s_waitcnt vmcnt(23)
	s_waitcnt lgkmcnt(5)
	v_mfma_f32_32x32x16_f16 v[2:17], v[114:117], v[94:97], v[2:17]
	s_waitcnt lgkmcnt(4)
	v_mfma_f32_32x32x16_f16 v[18:33], v[118:121], v[94:97], v[18:33]
	ds_read_b128 v[114:117], v162 offset:96
	ds_read_b128 v[118:121], v162 offset:8800
	global_load_dwordx4 v[94:97], v[158:159], off
	v_lshl_add_u64 v[158:159], v[158:159], 0, s[72:73]
	s_waitcnt vmcnt(23)
	s_waitcnt lgkmcnt(5)
	v_mfma_f32_32x32x16_f16 v[2:17], v[122:125], v[98:101], v[2:17]
	s_waitcnt lgkmcnt(4)
	v_mfma_f32_32x32x16_f16 v[18:33], v[126:129], v[98:101], v[18:33]
	ds_read_b128 v[122:125], v162 offset:128
	ds_read_b128 v[126:129], v162 offset:8832
	global_load_dwordx4 v[98:101], v[158:159], off
	v_lshl_add_u64 v[158:159], v[158:159], 0, s[72:73]
	s_waitcnt vmcnt(23)
	s_waitcnt lgkmcnt(5)
	v_mfma_f32_32x32x16_f16 v[2:17], v[130:133], v[102:105], v[2:17]
	s_waitcnt lgkmcnt(4)
	v_mfma_f32_32x32x16_f16 v[18:33], v[134:137], v[102:105], v[18:33]
	ds_read_b128 v[130:133], v162 offset:160
	ds_read_b128 v[134:137], v162 offset:8864
	global_load_dwordx4 v[102:105], v[158:159], off
	v_lshl_add_u64 v[158:159], v[158:159], 0, s[72:73]
	s_waitcnt vmcnt(23)
	s_waitcnt lgkmcnt(5)
	v_mfma_f32_32x32x16_f16 v[2:17], v[114:117], v[106:109], v[2:17]
	s_waitcnt lgkmcnt(4)
	v_mfma_f32_32x32x16_f16 v[18:33], v[118:121], v[106:109], v[18:33]
	ds_read_b128 v[114:117], v162 offset:192
	ds_read_b128 v[118:121], v162 offset:8896
	global_load_dwordx4 v[106:109], v[158:159], off
	v_lshl_add_u64 v[158:159], v[158:159], 0, s[72:73]
	s_waitcnt vmcnt(23)
	s_waitcnt lgkmcnt(5)
	v_mfma_f32_32x32x16_f16 v[2:17], v[122:125], v[142:145], v[2:17]
	s_waitcnt lgkmcnt(4)
	v_mfma_f32_32x32x16_f16 v[18:33], v[126:129], v[142:145], v[18:33]
	ds_read_b128 v[122:125], v162 offset:224
	ds_read_b128 v[126:129], v162 offset:8928
	global_load_dwordx4 v[142:145], v[158:159], off
	v_lshl_add_u64 v[158:159], v[158:159], 0, s[72:73]
	s_waitcnt vmcnt(23)
	s_waitcnt lgkmcnt(5)
	v_mfma_f32_32x32x16_f16 v[2:17], v[130:133], v[146:149], v[2:17]
	s_waitcnt lgkmcnt(4)
	v_mfma_f32_32x32x16_f16 v[18:33], v[134:137], v[146:149], v[18:33]
	global_load_dwordx4 v[146:149], v[158:159], off
	v_lshl_add_u64 v[158:159], v[158:159], 0, s[72:73]
	s_waitcnt vmcnt(23)
	s_waitcnt lgkmcnt(3)
	v_mfma_f32_32x32x16_f16 v[2:17], v[114:117], v[150:153], v[2:17]
	s_waitcnt lgkmcnt(2)
	v_mfma_f32_32x32x16_f16 v[18:33], v[118:121], v[150:153], v[18:33]
	global_load_dwordx4 v[150:153], v[158:159], off
	v_lshl_add_u64 v[158:159], v[158:159], 0, s[72:73]
	s_waitcnt vmcnt(23)
	s_waitcnt lgkmcnt(1)
	v_mfma_f32_32x32x16_f16 v[2:17], v[122:125], v[154:157], v[2:17]
	s_waitcnt lgkmcnt(0)
	v_mfma_f32_32x32x16_f16 v[18:33], v[126:129], v[154:157], v[18:33]
	global_load_dwordx4 v[154:157], v[158:159], off
	v_lshl_add_u64 v[158:159], v[158:159], 0, s[72:73]
	s_waitcnt lgkmcnt(0)
	s_barrier
	ds_read_b128 v[114:117], v162 offset:17408
	ds_read_b128 v[118:121], v162 offset:26112
	ds_read_b128 v[122:125], v162 offset:17440
	ds_read_b128 v[126:129], v162 offset:26144
	ds_read_b128 v[130:133], v162 offset:17472
	ds_read_b128 v[134:137], v162 offset:26176
	s_waitcnt vmcnt(23)
	s_waitcnt lgkmcnt(5)
	v_mfma_f32_32x32x16_f16 v[2:17], v[114:117], v[110:113], v[2:17]
	s_waitcnt lgkmcnt(4)
	v_mfma_f32_32x32x16_f16 v[18:33], v[118:121], v[110:113], v[18:33]
	ds_read_b128 v[114:117], v162 offset:17504
	ds_read_b128 v[118:121], v162 offset:26208
	global_load_dwordx4 v[110:113], v[158:159], off
	v_lshl_add_u64 v[158:159], v[158:159], 0, s[72:73]
	s_waitcnt vmcnt(23)
	s_waitcnt lgkmcnt(5)
	v_mfma_f32_32x32x16_f16 v[2:17], v[122:125], v[90:93], v[2:17]
	s_waitcnt lgkmcnt(4)
	v_mfma_f32_32x32x16_f16 v[18:33], v[126:129], v[90:93], v[18:33]
	ds_read_b128 v[122:125], v162 offset:17536
	ds_read_b128 v[126:129], v162 offset:26240
	global_load_dwordx4 v[90:93], v[158:159], off
	v_lshl_add_u64 v[158:159], v[158:159], 0, s[72:73]
	s_waitcnt vmcnt(23)
	s_waitcnt lgkmcnt(5)
	v_mfma_f32_32x32x16_f16 v[2:17], v[130:133], v[86:89], v[2:17]
	s_waitcnt lgkmcnt(4)
	v_mfma_f32_32x32x16_f16 v[18:33], v[134:137], v[86:89], v[18:33]
	ds_read_b128 v[130:133], v162 offset:17568
	ds_read_b128 v[134:137], v162 offset:26272
	global_load_dwordx4 v[86:89], v[158:159], off
	v_lshl_add_u64 v[158:159], v[158:159], 0, s[72:73]
	s_waitcnt vmcnt(23)
	s_waitcnt lgkmcnt(5)
	v_mfma_f32_32x32x16_f16 v[2:17], v[114:117], v[82:85], v[2:17]
	s_waitcnt lgkmcnt(4)
	v_mfma_f32_32x32x16_f16 v[18:33], v[118:121], v[82:85], v[18:33]
	ds_read_b128 v[114:117], v162 offset:17600
	ds_read_b128 v[118:121], v162 offset:26304
	global_load_dwordx4 v[82:85], v[158:159], off
	v_lshl_add_u64 v[158:159], v[158:159], 0, s[72:73]
	s_waitcnt vmcnt(23)
	s_waitcnt lgkmcnt(5)
	v_mfma_f32_32x32x16_f16 v[2:17], v[122:125], v[78:81], v[2:17]
	s_waitcnt lgkmcnt(4)
	v_mfma_f32_32x32x16_f16 v[18:33], v[126:129], v[78:81], v[18:33]
	ds_read_b128 v[122:125], v162 offset:17632
	ds_read_b128 v[126:129], v162 offset:26336
	global_load_dwordx4 v[78:81], v[158:159], off
	v_lshl_add_u64 v[158:159], v[158:159], 0, s[72:73]
	s_waitcnt vmcnt(23)
	s_waitcnt lgkmcnt(5)
	v_mfma_f32_32x32x16_f16 v[2:17], v[130:133], v[74:77], v[2:17]
	s_waitcnt lgkmcnt(4)
	v_mfma_f32_32x32x16_f16 v[18:33], v[134:137], v[74:77], v[18:33]
	global_load_dwordx4 v[74:77], v[158:159], off
	v_lshl_add_u64 v[158:159], v[158:159], 0, s[72:73]
	s_waitcnt vmcnt(23)
	s_waitcnt lgkmcnt(3)
	v_mfma_f32_32x32x16_f16 v[2:17], v[114:117], v[70:73], v[2:17]
	s_waitcnt lgkmcnt(2)
	v_mfma_f32_32x32x16_f16 v[18:33], v[118:121], v[70:73], v[18:33]
	global_load_dwordx4 v[70:73], v[158:159], off
	v_lshl_add_u64 v[158:159], v[158:159], 0, s[72:73]
	s_waitcnt vmcnt(23)
	s_waitcnt lgkmcnt(1)
	v_mfma_f32_32x32x16_f16 v[2:17], v[122:125], v[66:69], v[2:17]
	s_waitcnt lgkmcnt(0)
	v_mfma_f32_32x32x16_f16 v[18:33], v[126:129], v[66:69], v[18:33]
	global_load_dwordx4 v[66:69], v[158:159], off
	v_lshl_add_u64 v[158:159], v[158:159], 0, s[72:73]
	s_waitcnt lgkmcnt(0)
	s_barrier
	ds_read_b128 v[114:117], v162 offset:34816
	ds_read_b128 v[118:121], v162 offset:43520
	ds_read_b128 v[122:125], v162 offset:34848
	ds_read_b128 v[126:129], v162 offset:43552
	ds_read_b128 v[130:133], v162 offset:34880
	ds_read_b128 v[134:137], v162 offset:43584
	s_waitcnt vmcnt(23)
	s_waitcnt lgkmcnt(5)
	v_mfma_f32_32x32x16_f16 v[2:17], v[114:117], v[62:65], v[2:17]
	s_waitcnt lgkmcnt(4)
	v_mfma_f32_32x32x16_f16 v[18:33], v[118:121], v[62:65], v[18:33]
	ds_read_b128 v[114:117], v162 offset:34912
	ds_read_b128 v[118:121], v162 offset:43616
	global_load_dwordx4 v[62:65], v[158:159], off
	v_lshl_add_u64 v[158:159], v[158:159], 0, s[72:73]
	s_waitcnt vmcnt(23)
	s_waitcnt lgkmcnt(5)
	v_mfma_f32_32x32x16_f16 v[2:17], v[122:125], v[58:61], v[2:17]
	s_waitcnt lgkmcnt(4)
	v_mfma_f32_32x32x16_f16 v[18:33], v[126:129], v[58:61], v[18:33]
	ds_read_b128 v[122:125], v162 offset:34944
	ds_read_b128 v[126:129], v162 offset:43648
	global_load_dwordx4 v[58:61], v[158:159], off
	v_lshl_add_u64 v[158:159], v[158:159], 0, s[72:73]
	s_waitcnt vmcnt(23)
	s_waitcnt lgkmcnt(5)
	v_mfma_f32_32x32x16_f16 v[2:17], v[130:133], v[54:57], v[2:17]
	s_waitcnt lgkmcnt(4)
	v_mfma_f32_32x32x16_f16 v[18:33], v[134:137], v[54:57], v[18:33]
	ds_read_b128 v[130:133], v162 offset:34976
	ds_read_b128 v[134:137], v162 offset:43680
	global_load_dwordx4 v[54:57], v[158:159], off
	v_lshl_add_u64 v[158:159], v[158:159], 0, s[72:73]
	s_waitcnt vmcnt(23)
	s_waitcnt lgkmcnt(5)
	v_mfma_f32_32x32x16_f16 v[2:17], v[114:117], v[50:53], v[2:17]
	s_waitcnt lgkmcnt(4)
	v_mfma_f32_32x32x16_f16 v[18:33], v[118:121], v[50:53], v[18:33]
	ds_read_b128 v[114:117], v162 offset:35008
	ds_read_b128 v[118:121], v162 offset:43712
	global_load_dwordx4 v[50:53], v[158:159], off
	v_lshl_add_u64 v[158:159], v[158:159], 0, s[72:73]
	s_waitcnt vmcnt(23)
	s_waitcnt lgkmcnt(5)
	v_mfma_f32_32x32x16_f16 v[2:17], v[122:125], v[46:49], v[2:17]
	s_waitcnt lgkmcnt(4)
	v_mfma_f32_32x32x16_f16 v[18:33], v[126:129], v[46:49], v[18:33]
	ds_read_b128 v[122:125], v162 offset:35040
	ds_read_b128 v[126:129], v162 offset:43744
	global_load_dwordx4 v[46:49], v[158:159], off
	v_lshl_add_u64 v[158:159], v[158:159], 0, s[72:73]
	s_waitcnt vmcnt(23)
	s_waitcnt lgkmcnt(5)
	v_mfma_f32_32x32x16_f16 v[2:17], v[130:133], v[42:45], v[2:17]
	s_waitcnt lgkmcnt(4)
	v_mfma_f32_32x32x16_f16 v[18:33], v[134:137], v[42:45], v[18:33]
	global_load_dwordx4 v[42:45], v[158:159], off
	v_lshl_add_u64 v[158:159], v[158:159], 0, s[72:73]
	s_waitcnt vmcnt(23)
	s_waitcnt lgkmcnt(3)
	v_mfma_f32_32x32x16_f16 v[2:17], v[114:117], v[38:41], v[2:17]
	s_waitcnt lgkmcnt(2)
	v_mfma_f32_32x32x16_f16 v[18:33], v[118:121], v[38:41], v[18:33]
	global_load_dwordx4 v[38:41], v[158:159], off
	v_lshl_add_u64 v[158:159], v[158:159], 0, s[72:73]
	s_waitcnt vmcnt(23)
	s_waitcnt lgkmcnt(1)
	v_mfma_f32_32x32x16_f16 v[2:17], v[122:125], v[34:37], v[2:17]
	s_waitcnt lgkmcnt(0)
	v_mfma_f32_32x32x16_f16 v[18:33], v[126:129], v[34:37], v[18:33]
	global_load_dwordx4 v[34:37], v[158:159], off
	v_lshl_add_u64 v[158:159], v[158:159], 0, s[72:73]
	s_waitcnt lgkmcnt(0)
	s_barrier
	ds_read_b128 v[114:117], v162 offset:52224
	ds_read_b128 v[118:121], v162 offset:60928
	ds_read_b128 v[122:125], v162 offset:52256
	ds_read_b128 v[126:129], v162 offset:60960
	ds_read_b128 v[130:133], v162 offset:52288
	ds_read_b128 v[134:137], v162 offset:60992
	s_waitcnt vmcnt(23)
	s_waitcnt lgkmcnt(5)
	v_mfma_f32_32x32x16_f16 v[2:17], v[114:117], v[94:97], v[2:17]
	s_waitcnt lgkmcnt(4)
	v_mfma_f32_32x32x16_f16 v[18:33], v[118:121], v[94:97], v[18:33]
	ds_read_b128 v[114:117], v162 offset:52320
	ds_read_b128 v[118:121], v162 offset:61024
	global_load_dwordx4 v[94:97], v[158:159], off
	v_lshl_add_u64 v[158:159], v[158:159], 0, s[72:73]
	s_waitcnt vmcnt(23)
	s_waitcnt lgkmcnt(5)
	v_mfma_f32_32x32x16_f16 v[2:17], v[122:125], v[98:101], v[2:17]
	s_waitcnt lgkmcnt(4)
	v_mfma_f32_32x32x16_f16 v[18:33], v[126:129], v[98:101], v[18:33]
	ds_read_b128 v[122:125], v162 offset:52352
	ds_read_b128 v[126:129], v162 offset:61056
	global_load_dwordx4 v[98:101], v[158:159], off
	v_lshl_add_u64 v[158:159], v[158:159], 0, s[72:73]
	s_waitcnt vmcnt(23)
	s_waitcnt lgkmcnt(5)
	v_mfma_f32_32x32x16_f16 v[2:17], v[130:133], v[102:105], v[2:17]
	s_waitcnt lgkmcnt(4)
	v_mfma_f32_32x32x16_f16 v[18:33], v[134:137], v[102:105], v[18:33]
	ds_read_b128 v[130:133], v162 offset:52384
	ds_read_b128 v[134:137], v162 offset:61088
	global_load_dwordx4 v[102:105], v[158:159], off
	v_lshl_add_u64 v[158:159], v[158:159], 0, s[72:73]
	s_waitcnt vmcnt(23)
	s_waitcnt lgkmcnt(5)
	v_mfma_f32_32x32x16_f16 v[2:17], v[114:117], v[106:109], v[2:17]
	s_waitcnt lgkmcnt(4)
	v_mfma_f32_32x32x16_f16 v[18:33], v[118:121], v[106:109], v[18:33]
	ds_read_b128 v[114:117], v162 offset:52416
	ds_read_b128 v[118:121], v162 offset:61120
	global_load_dwordx4 v[106:109], v[158:159], off
	v_lshl_add_u64 v[158:159], v[158:159], 0, s[72:73]
	s_waitcnt vmcnt(23)
	s_waitcnt lgkmcnt(5)
	v_mfma_f32_32x32x16_f16 v[2:17], v[122:125], v[142:145], v[2:17]
	s_waitcnt lgkmcnt(4)
	v_mfma_f32_32x32x16_f16 v[18:33], v[126:129], v[142:145], v[18:33]
	ds_read_b128 v[122:125], v162 offset:52448
	ds_read_b128 v[126:129], v162 offset:61152
	global_load_dwordx4 v[142:145], v[158:159], off
	v_lshl_add_u64 v[158:159], v[158:159], 0, s[72:73]
	s_waitcnt vmcnt(23)
	s_waitcnt lgkmcnt(5)
	v_mfma_f32_32x32x16_f16 v[2:17], v[130:133], v[146:149], v[2:17]
	s_waitcnt lgkmcnt(4)
	v_mfma_f32_32x32x16_f16 v[18:33], v[134:137], v[146:149], v[18:33]
	global_load_dwordx4 v[146:149], v[158:159], off
	v_lshl_add_u64 v[158:159], v[158:159], 0, s[72:73]
	s_waitcnt vmcnt(23)
	s_waitcnt lgkmcnt(3)
	v_mfma_f32_32x32x16_f16 v[2:17], v[114:117], v[150:153], v[2:17]
	s_waitcnt lgkmcnt(2)
	v_mfma_f32_32x32x16_f16 v[18:33], v[118:121], v[150:153], v[18:33]
	global_load_dwordx4 v[150:153], v[158:159], off
	v_lshl_add_u64 v[158:159], v[158:159], 0, s[72:73]
	s_waitcnt vmcnt(23)
	s_waitcnt lgkmcnt(1)
	v_mfma_f32_32x32x16_f16 v[2:17], v[122:125], v[154:157], v[2:17]
	s_waitcnt lgkmcnt(0)
	v_mfma_f32_32x32x16_f16 v[18:33], v[126:129], v[154:157], v[18:33]
	global_load_dwordx4 v[154:157], v[158:159], off
	v_lshl_add_u64 v[158:159], v[158:159], 0, s[72:73]
	s_waitcnt lgkmcnt(0)
	s_barrier
	ds_read_b128 v[114:117], v162 offset:0
	ds_read_b128 v[118:121], v162 offset:8704
	ds_read_b128 v[122:125], v162 offset:32
	ds_read_b128 v[126:129], v162 offset:8736
	ds_read_b128 v[130:133], v162 offset:64
	ds_read_b128 v[134:137], v162 offset:8768
	s_waitcnt vmcnt(23)
	s_waitcnt lgkmcnt(5)
	v_mfma_f32_32x32x16_f16 v[2:17], v[114:117], v[110:113], v[2:17]
	s_waitcnt lgkmcnt(4)
	v_mfma_f32_32x32x16_f16 v[18:33], v[118:121], v[110:113], v[18:33]
	ds_read_b128 v[114:117], v162 offset:96
	ds_read_b128 v[118:121], v162 offset:8800
	global_load_dwordx4 v[110:113], v[158:159], off
	v_lshl_add_u64 v[158:159], v[158:159], 0, s[72:73]
	s_waitcnt vmcnt(23)
	s_waitcnt lgkmcnt(5)
	v_mfma_f32_32x32x16_f16 v[2:17], v[122:125], v[90:93], v[2:17]
	s_waitcnt lgkmcnt(4)
	v_mfma_f32_32x32x16_f16 v[18:33], v[126:129], v[90:93], v[18:33]
	ds_read_b128 v[122:125], v162 offset:128
	ds_read_b128 v[126:129], v162 offset:8832
	global_load_dwordx4 v[90:93], v[158:159], off
	v_lshl_add_u64 v[158:159], v[158:159], 0, s[72:73]
	s_waitcnt vmcnt(23)
	s_waitcnt lgkmcnt(5)
	v_mfma_f32_32x32x16_f16 v[2:17], v[130:133], v[86:89], v[2:17]
	s_waitcnt lgkmcnt(4)
	v_mfma_f32_32x32x16_f16 v[18:33], v[134:137], v[86:89], v[18:33]
	ds_read_b128 v[130:133], v162 offset:160
	ds_read_b128 v[134:137], v162 offset:8864
	global_load_dwordx4 v[86:89], v[158:159], off
	v_lshl_add_u64 v[158:159], v[158:159], 0, s[72:73]
	s_waitcnt vmcnt(23)
	s_waitcnt lgkmcnt(5)
	v_mfma_f32_32x32x16_f16 v[2:17], v[114:117], v[82:85], v[2:17]
	s_waitcnt lgkmcnt(4)
	v_mfma_f32_32x32x16_f16 v[18:33], v[118:121], v[82:85], v[18:33]
	ds_read_b128 v[114:117], v162 offset:192
	ds_read_b128 v[118:121], v162 offset:8896
	global_load_dwordx4 v[82:85], v[158:159], off
	v_lshl_add_u64 v[158:159], v[158:159], 0, s[72:73]
	s_waitcnt vmcnt(23)
	s_waitcnt lgkmcnt(5)
	v_mfma_f32_32x32x16_f16 v[2:17], v[122:125], v[78:81], v[2:17]
	s_waitcnt lgkmcnt(4)
	v_mfma_f32_32x32x16_f16 v[18:33], v[126:129], v[78:81], v[18:33]
	ds_read_b128 v[122:125], v162 offset:224
	ds_read_b128 v[126:129], v162 offset:8928
	global_load_dwordx4 v[78:81], v[158:159], off
	v_lshl_add_u64 v[158:159], v[158:159], 0, s[72:73]
	s_waitcnt vmcnt(23)
	s_waitcnt lgkmcnt(5)
	v_mfma_f32_32x32x16_f16 v[2:17], v[130:133], v[74:77], v[2:17]
	s_waitcnt lgkmcnt(4)
	v_mfma_f32_32x32x16_f16 v[18:33], v[134:137], v[74:77], v[18:33]
	global_load_dwordx4 v[74:77], v[158:159], off
	v_lshl_add_u64 v[158:159], v[158:159], 0, s[72:73]
	s_waitcnt vmcnt(23)
	s_waitcnt lgkmcnt(3)
	v_mfma_f32_32x32x16_f16 v[2:17], v[114:117], v[70:73], v[2:17]
	s_waitcnt lgkmcnt(2)
	v_mfma_f32_32x32x16_f16 v[18:33], v[118:121], v[70:73], v[18:33]
	global_load_dwordx4 v[70:73], v[158:159], off
	v_lshl_add_u64 v[158:159], v[158:159], 0, s[72:73]
	s_waitcnt vmcnt(23)
	s_waitcnt lgkmcnt(1)
	v_mfma_f32_32x32x16_f16 v[2:17], v[122:125], v[66:69], v[2:17]
	s_waitcnt lgkmcnt(0)
	v_mfma_f32_32x32x16_f16 v[18:33], v[126:129], v[66:69], v[18:33]
	global_load_dwordx4 v[66:69], v[158:159], off
	v_lshl_add_u64 v[158:159], v[158:159], 0, s[72:73]
	s_waitcnt lgkmcnt(0)
	s_barrier
	ds_read_b128 v[114:117], v162 offset:17408
	ds_read_b128 v[118:121], v162 offset:26112
	ds_read_b128 v[122:125], v162 offset:17440
	ds_read_b128 v[126:129], v162 offset:26144
	ds_read_b128 v[130:133], v162 offset:17472
	ds_read_b128 v[134:137], v162 offset:26176
	s_waitcnt vmcnt(23)
	s_waitcnt lgkmcnt(5)
	v_mfma_f32_32x32x16_f16 v[2:17], v[114:117], v[62:65], v[2:17]
	s_waitcnt lgkmcnt(4)
	v_mfma_f32_32x32x16_f16 v[18:33], v[118:121], v[62:65], v[18:33]
	ds_read_b128 v[114:117], v162 offset:17504
	ds_read_b128 v[118:121], v162 offset:26208
	global_load_dwordx4 v[62:65], v[158:159], off
	v_lshl_add_u64 v[158:159], v[158:159], 0, s[72:73]
	s_waitcnt vmcnt(23)
	s_waitcnt lgkmcnt(5)
	v_mfma_f32_32x32x16_f16 v[2:17], v[122:125], v[58:61], v[2:17]
	s_waitcnt lgkmcnt(4)
	v_mfma_f32_32x32x16_f16 v[18:33], v[126:129], v[58:61], v[18:33]
	ds_read_b128 v[122:125], v162 offset:17536
	ds_read_b128 v[126:129], v162 offset:26240
	global_load_dwordx4 v[58:61], v[158:159], off
	v_lshl_add_u64 v[158:159], v[158:159], 0, s[72:73]
	s_waitcnt vmcnt(23)
	s_waitcnt lgkmcnt(5)
	v_mfma_f32_32x32x16_f16 v[2:17], v[130:133], v[54:57], v[2:17]
	s_waitcnt lgkmcnt(4)
	v_mfma_f32_32x32x16_f16 v[18:33], v[134:137], v[54:57], v[18:33]
	ds_read_b128 v[130:133], v162 offset:17568
	ds_read_b128 v[134:137], v162 offset:26272
	global_load_dwordx4 v[54:57], v[158:159], off
	v_lshl_add_u64 v[158:159], v[158:159], 0, s[72:73]
	s_waitcnt vmcnt(23)
	s_waitcnt lgkmcnt(5)
	v_mfma_f32_32x32x16_f16 v[2:17], v[114:117], v[50:53], v[2:17]
	s_waitcnt lgkmcnt(4)
	v_mfma_f32_32x32x16_f16 v[18:33], v[118:121], v[50:53], v[18:33]
	ds_read_b128 v[114:117], v162 offset:17600
	ds_read_b128 v[118:121], v162 offset:26304
	global_load_dwordx4 v[50:53], v[158:159], off
	v_lshl_add_u64 v[158:159], v[158:159], 0, s[72:73]
	s_waitcnt vmcnt(23)
	s_waitcnt lgkmcnt(5)
	v_mfma_f32_32x32x16_f16 v[2:17], v[122:125], v[46:49], v[2:17]
	s_waitcnt lgkmcnt(4)
	v_mfma_f32_32x32x16_f16 v[18:33], v[126:129], v[46:49], v[18:33]
	ds_read_b128 v[122:125], v162 offset:17632
	ds_read_b128 v[126:129], v162 offset:26336
	global_load_dwordx4 v[46:49], v[158:159], off
	v_lshl_add_u64 v[158:159], v[158:159], 0, s[72:73]
	s_waitcnt vmcnt(23)
	s_waitcnt lgkmcnt(5)
	v_mfma_f32_32x32x16_f16 v[2:17], v[130:133], v[42:45], v[2:17]
	s_waitcnt lgkmcnt(4)
	v_mfma_f32_32x32x16_f16 v[18:33], v[134:137], v[42:45], v[18:33]
	global_load_dwordx4 v[42:45], v[158:159], off
	v_lshl_add_u64 v[158:159], v[158:159], 0, s[72:73]
	s_waitcnt vmcnt(23)
	s_waitcnt lgkmcnt(3)
	v_mfma_f32_32x32x16_f16 v[2:17], v[114:117], v[38:41], v[2:17]
	s_waitcnt lgkmcnt(2)
	v_mfma_f32_32x32x16_f16 v[18:33], v[118:121], v[38:41], v[18:33]
	global_load_dwordx4 v[38:41], v[158:159], off
	v_lshl_add_u64 v[158:159], v[158:159], 0, s[72:73]
	s_waitcnt vmcnt(23)
	s_waitcnt lgkmcnt(1)
	v_mfma_f32_32x32x16_f16 v[2:17], v[122:125], v[34:37], v[2:17]
	s_waitcnt lgkmcnt(0)
	v_mfma_f32_32x32x16_f16 v[18:33], v[126:129], v[34:37], v[18:33]
	global_load_dwordx4 v[34:37], v[158:159], off
	v_lshl_add_u64 v[158:159], v[158:159], 0, s[72:73]
	s_waitcnt lgkmcnt(0)
	s_barrier
	ds_read_b128 v[114:117], v162 offset:34816
	ds_read_b128 v[118:121], v162 offset:43520
	ds_read_b128 v[122:125], v162 offset:34848
	ds_read_b128 v[126:129], v162 offset:43552
	ds_read_b128 v[130:133], v162 offset:34880
	ds_read_b128 v[134:137], v162 offset:43584
	s_waitcnt vmcnt(23)
	s_waitcnt lgkmcnt(5)
	v_mfma_f32_32x32x16_f16 v[2:17], v[114:117], v[94:97], v[2:17]
	s_waitcnt lgkmcnt(4)
	v_mfma_f32_32x32x16_f16 v[18:33], v[118:121], v[94:97], v[18:33]
	ds_read_b128 v[114:117], v162 offset:34912
	ds_read_b128 v[118:121], v162 offset:43616
	global_load_dwordx4 v[94:97], v[158:159], off
	v_lshl_add_u64 v[158:159], v[158:159], 0, s[72:73]
	s_waitcnt vmcnt(23)
	s_waitcnt lgkmcnt(5)
	v_mfma_f32_32x32x16_f16 v[2:17], v[122:125], v[98:101], v[2:17]
	s_waitcnt lgkmcnt(4)
	v_mfma_f32_32x32x16_f16 v[18:33], v[126:129], v[98:101], v[18:33]
	ds_read_b128 v[122:125], v162 offset:34944
	ds_read_b128 v[126:129], v162 offset:43648
	global_load_dwordx4 v[98:101], v[158:159], off
	v_lshl_add_u64 v[158:159], v[158:159], 0, s[72:73]
	s_waitcnt vmcnt(23)
	s_waitcnt lgkmcnt(5)
	v_mfma_f32_32x32x16_f16 v[2:17], v[130:133], v[102:105], v[2:17]
	s_waitcnt lgkmcnt(4)
	v_mfma_f32_32x32x16_f16 v[18:33], v[134:137], v[102:105], v[18:33]
	ds_read_b128 v[130:133], v162 offset:34976
	ds_read_b128 v[134:137], v162 offset:43680
	global_load_dwordx4 v[102:105], v[158:159], off
	v_lshl_add_u64 v[158:159], v[158:159], 0, s[72:73]
	s_waitcnt vmcnt(23)
	s_waitcnt lgkmcnt(5)
	v_mfma_f32_32x32x16_f16 v[2:17], v[114:117], v[106:109], v[2:17]
	s_waitcnt lgkmcnt(4)
	v_mfma_f32_32x32x16_f16 v[18:33], v[118:121], v[106:109], v[18:33]
	ds_read_b128 v[114:117], v162 offset:35008
	ds_read_b128 v[118:121], v162 offset:43712
	global_load_dwordx4 v[106:109], v[158:159], off
	v_lshl_add_u64 v[158:159], v[158:159], 0, s[72:73]
	s_waitcnt vmcnt(23)
	s_waitcnt lgkmcnt(5)
	v_mfma_f32_32x32x16_f16 v[2:17], v[122:125], v[142:145], v[2:17]
	s_waitcnt lgkmcnt(4)
	v_mfma_f32_32x32x16_f16 v[18:33], v[126:129], v[142:145], v[18:33]
	ds_read_b128 v[122:125], v162 offset:35040
	ds_read_b128 v[126:129], v162 offset:43744
	global_load_dwordx4 v[142:145], v[158:159], off
	v_lshl_add_u64 v[158:159], v[158:159], 0, s[72:73]
	s_waitcnt vmcnt(23)
	s_waitcnt lgkmcnt(5)
	v_mfma_f32_32x32x16_f16 v[2:17], v[130:133], v[146:149], v[2:17]
	s_waitcnt lgkmcnt(4)
	v_mfma_f32_32x32x16_f16 v[18:33], v[134:137], v[146:149], v[18:33]
	global_load_dwordx4 v[146:149], v[158:159], off
	v_lshl_add_u64 v[158:159], v[158:159], 0, s[72:73]
	s_waitcnt vmcnt(23)
	s_waitcnt lgkmcnt(3)
	v_mfma_f32_32x32x16_f16 v[2:17], v[114:117], v[150:153], v[2:17]
	s_waitcnt lgkmcnt(2)
	v_mfma_f32_32x32x16_f16 v[18:33], v[118:121], v[150:153], v[18:33]
	global_load_dwordx4 v[150:153], v[158:159], off
	v_lshl_add_u64 v[158:159], v[158:159], 0, s[72:73]
	s_waitcnt vmcnt(23)
	s_waitcnt lgkmcnt(1)
	v_mfma_f32_32x32x16_f16 v[2:17], v[122:125], v[154:157], v[2:17]
	s_waitcnt lgkmcnt(0)
	v_mfma_f32_32x32x16_f16 v[18:33], v[126:129], v[154:157], v[18:33]
	global_load_dwordx4 v[154:157], v[158:159], off
	v_lshl_add_u64 v[158:159], v[158:159], 0, s[72:73]
	s_waitcnt lgkmcnt(0)
	s_barrier
	ds_read_b128 v[114:117], v162 offset:52224
	ds_read_b128 v[118:121], v162 offset:60928
	ds_read_b128 v[122:125], v162 offset:52256
	ds_read_b128 v[126:129], v162 offset:60960
	ds_read_b128 v[130:133], v162 offset:52288
	ds_read_b128 v[134:137], v162 offset:60992
	s_waitcnt vmcnt(23)
	s_waitcnt lgkmcnt(5)
	v_mfma_f32_32x32x16_f16 v[2:17], v[114:117], v[110:113], v[2:17]
	s_waitcnt lgkmcnt(4)
	v_mfma_f32_32x32x16_f16 v[18:33], v[118:121], v[110:113], v[18:33]
	ds_read_b128 v[114:117], v162 offset:52320
	ds_read_b128 v[118:121], v162 offset:61024
	global_load_dwordx4 v[110:113], v[158:159], off
	v_lshl_add_u64 v[158:159], v[158:159], 0, s[72:73]
	s_waitcnt vmcnt(23)
	s_waitcnt lgkmcnt(5)
	v_mfma_f32_32x32x16_f16 v[2:17], v[122:125], v[90:93], v[2:17]
	s_waitcnt lgkmcnt(4)
	v_mfma_f32_32x32x16_f16 v[18:33], v[126:129], v[90:93], v[18:33]
	ds_read_b128 v[122:125], v162 offset:52352
	ds_read_b128 v[126:129], v162 offset:61056
	global_load_dwordx4 v[90:93], v[158:159], off
	v_lshl_add_u64 v[158:159], v[158:159], 0, s[72:73]
	s_waitcnt vmcnt(23)
	s_waitcnt lgkmcnt(5)
	v_mfma_f32_32x32x16_f16 v[2:17], v[130:133], v[86:89], v[2:17]
	s_waitcnt lgkmcnt(4)
	v_mfma_f32_32x32x16_f16 v[18:33], v[134:137], v[86:89], v[18:33]
	ds_read_b128 v[130:133], v162 offset:52384
	ds_read_b128 v[134:137], v162 offset:61088
	global_load_dwordx4 v[86:89], v[158:159], off
	v_lshl_add_u64 v[158:159], v[158:159], 0, s[72:73]
	s_waitcnt vmcnt(23)
	s_waitcnt lgkmcnt(5)
	v_mfma_f32_32x32x16_f16 v[2:17], v[114:117], v[82:85], v[2:17]
	s_waitcnt lgkmcnt(4)
	v_mfma_f32_32x32x16_f16 v[18:33], v[118:121], v[82:85], v[18:33]
	ds_read_b128 v[114:117], v162 offset:52416
	ds_read_b128 v[118:121], v162 offset:61120
	global_load_dwordx4 v[82:85], v[158:159], off
	v_lshl_add_u64 v[158:159], v[158:159], 0, s[72:73]
	s_waitcnt vmcnt(23)
	s_waitcnt lgkmcnt(5)
	v_mfma_f32_32x32x16_f16 v[2:17], v[122:125], v[78:81], v[2:17]
	s_waitcnt lgkmcnt(4)
	v_mfma_f32_32x32x16_f16 v[18:33], v[126:129], v[78:81], v[18:33]
	ds_read_b128 v[122:125], v162 offset:52448
	ds_read_b128 v[126:129], v162 offset:61152
	global_load_dwordx4 v[78:81], v[158:159], off
	v_lshl_add_u64 v[158:159], v[158:159], 0, s[72:73]
	s_waitcnt vmcnt(23)
	s_waitcnt lgkmcnt(5)
	v_mfma_f32_32x32x16_f16 v[2:17], v[130:133], v[74:77], v[2:17]
	s_waitcnt lgkmcnt(4)
	v_mfma_f32_32x32x16_f16 v[18:33], v[134:137], v[74:77], v[18:33]
	global_load_dwordx4 v[74:77], v[158:159], off
	v_lshl_add_u64 v[158:159], v[158:159], 0, s[72:73]
	s_waitcnt vmcnt(23)
	s_waitcnt lgkmcnt(3)
	v_mfma_f32_32x32x16_f16 v[2:17], v[114:117], v[70:73], v[2:17]
	s_waitcnt lgkmcnt(2)
	v_mfma_f32_32x32x16_f16 v[18:33], v[118:121], v[70:73], v[18:33]
	global_load_dwordx4 v[70:73], v[158:159], off
	v_lshl_add_u64 v[158:159], v[158:159], 0, s[72:73]
	s_waitcnt vmcnt(23)
	s_waitcnt lgkmcnt(1)
	v_mfma_f32_32x32x16_f16 v[2:17], v[122:125], v[66:69], v[2:17]
	s_waitcnt lgkmcnt(0)
	v_mfma_f32_32x32x16_f16 v[18:33], v[126:129], v[66:69], v[18:33]
	global_load_dwordx4 v[66:69], v[158:159], off
	v_lshl_add_u64 v[158:159], v[158:159], 0, s[72:73]
	s_waitcnt lgkmcnt(0)
	s_barrier
	ds_read_b128 v[114:117], v162 offset:0
	ds_read_b128 v[118:121], v162 offset:8704
	ds_read_b128 v[122:125], v162 offset:32
	ds_read_b128 v[126:129], v162 offset:8736
	ds_read_b128 v[130:133], v162 offset:64
	ds_read_b128 v[134:137], v162 offset:8768
	s_waitcnt vmcnt(23)
	s_waitcnt lgkmcnt(5)
	v_mfma_f32_32x32x16_f16 v[2:17], v[114:117], v[62:65], v[2:17]
	s_waitcnt lgkmcnt(4)
	v_mfma_f32_32x32x16_f16 v[18:33], v[118:121], v[62:65], v[18:33]
	ds_read_b128 v[114:117], v162 offset:96
	ds_read_b128 v[118:121], v162 offset:8800
	global_load_dwordx4 v[62:65], v[158:159], off
	v_lshl_add_u64 v[158:159], v[158:159], 0, s[72:73]
	s_waitcnt vmcnt(23)
	s_waitcnt lgkmcnt(5)
	v_mfma_f32_32x32x16_f16 v[2:17], v[122:125], v[58:61], v[2:17]
	s_waitcnt lgkmcnt(4)
	v_mfma_f32_32x32x16_f16 v[18:33], v[126:129], v[58:61], v[18:33]
	ds_read_b128 v[122:125], v162 offset:128
	ds_read_b128 v[126:129], v162 offset:8832
	global_load_dwordx4 v[58:61], v[158:159], off
	v_lshl_add_u64 v[158:159], v[158:159], 0, s[72:73]
	s_waitcnt vmcnt(23)
	s_waitcnt lgkmcnt(5)
	v_mfma_f32_32x32x16_f16 v[2:17], v[130:133], v[54:57], v[2:17]
	s_waitcnt lgkmcnt(4)
	v_mfma_f32_32x32x16_f16 v[18:33], v[134:137], v[54:57], v[18:33]
	ds_read_b128 v[130:133], v162 offset:160
	ds_read_b128 v[134:137], v162 offset:8864
	global_load_dwordx4 v[54:57], v[158:159], off
	v_lshl_add_u64 v[158:159], v[158:159], 0, s[72:73]
	s_waitcnt vmcnt(23)
	s_waitcnt lgkmcnt(5)
	v_mfma_f32_32x32x16_f16 v[2:17], v[114:117], v[50:53], v[2:17]
	s_waitcnt lgkmcnt(4)
	v_mfma_f32_32x32x16_f16 v[18:33], v[118:121], v[50:53], v[18:33]
	ds_read_b128 v[114:117], v162 offset:192
	ds_read_b128 v[118:121], v162 offset:8896
	global_load_dwordx4 v[50:53], v[158:159], off
	v_lshl_add_u64 v[158:159], v[158:159], 0, s[72:73]
	s_waitcnt vmcnt(23)
	s_waitcnt lgkmcnt(5)
	v_mfma_f32_32x32x16_f16 v[2:17], v[122:125], v[46:49], v[2:17]
	s_waitcnt lgkmcnt(4)
	v_mfma_f32_32x32x16_f16 v[18:33], v[126:129], v[46:49], v[18:33]
	ds_read_b128 v[122:125], v162 offset:224
	ds_read_b128 v[126:129], v162 offset:8928
	global_load_dwordx4 v[46:49], v[158:159], off
	v_lshl_add_u64 v[158:159], v[158:159], 0, s[72:73]
	s_waitcnt vmcnt(23)
	s_waitcnt lgkmcnt(5)
	v_mfma_f32_32x32x16_f16 v[2:17], v[130:133], v[42:45], v[2:17]
	s_waitcnt lgkmcnt(4)
	v_mfma_f32_32x32x16_f16 v[18:33], v[134:137], v[42:45], v[18:33]
	global_load_dwordx4 v[42:45], v[158:159], off
	v_lshl_add_u64 v[158:159], v[158:159], 0, s[72:73]
	s_waitcnt vmcnt(23)
	s_waitcnt lgkmcnt(3)
	v_mfma_f32_32x32x16_f16 v[2:17], v[114:117], v[38:41], v[2:17]
	s_waitcnt lgkmcnt(2)
	v_mfma_f32_32x32x16_f16 v[18:33], v[118:121], v[38:41], v[18:33]
	global_load_dwordx4 v[38:41], v[158:159], off
	v_lshl_add_u64 v[158:159], v[158:159], 0, s[72:73]
	s_waitcnt vmcnt(23)
	s_waitcnt lgkmcnt(1)
	v_mfma_f32_32x32x16_f16 v[2:17], v[122:125], v[34:37], v[2:17]
	s_waitcnt lgkmcnt(0)
	v_mfma_f32_32x32x16_f16 v[18:33], v[126:129], v[34:37], v[18:33]
	global_load_dwordx4 v[34:37], v[158:159], off
	v_lshl_add_u64 v[158:159], v[158:159], 0, s[72:73]
	s_waitcnt lgkmcnt(0)
	s_barrier
	ds_read_b128 v[114:117], v162 offset:17408
	ds_read_b128 v[118:121], v162 offset:26112
	ds_read_b128 v[122:125], v162 offset:17440
	ds_read_b128 v[126:129], v162 offset:26144
	ds_read_b128 v[130:133], v162 offset:17472
	ds_read_b128 v[134:137], v162 offset:26176
	s_waitcnt vmcnt(23)
	s_waitcnt lgkmcnt(5)
	v_mfma_f32_32x32x16_f16 v[2:17], v[114:117], v[94:97], v[2:17]
	s_waitcnt lgkmcnt(4)
	v_mfma_f32_32x32x16_f16 v[18:33], v[118:121], v[94:97], v[18:33]
	ds_read_b128 v[114:117], v162 offset:17504
	ds_read_b128 v[118:121], v162 offset:26208
	global_load_dwordx4 v[94:97], v[158:159], off
	v_lshl_add_u64 v[158:159], v[158:159], 0, s[72:73]
	s_waitcnt vmcnt(23)
	s_waitcnt lgkmcnt(5)
	v_mfma_f32_32x32x16_f16 v[2:17], v[122:125], v[98:101], v[2:17]
	s_waitcnt lgkmcnt(4)
	v_mfma_f32_32x32x16_f16 v[18:33], v[126:129], v[98:101], v[18:33]
	ds_read_b128 v[122:125], v162 offset:17536
	ds_read_b128 v[126:129], v162 offset:26240
	global_load_dwordx4 v[98:101], v[158:159], off
	v_lshl_add_u64 v[158:159], v[158:159], 0, s[72:73]
	s_waitcnt vmcnt(23)
	s_waitcnt lgkmcnt(5)
	v_mfma_f32_32x32x16_f16 v[2:17], v[130:133], v[102:105], v[2:17]
	s_waitcnt lgkmcnt(4)
	v_mfma_f32_32x32x16_f16 v[18:33], v[134:137], v[102:105], v[18:33]
	ds_read_b128 v[130:133], v162 offset:17568
	ds_read_b128 v[134:137], v162 offset:26272
	global_load_dwordx4 v[102:105], v[158:159], off
	v_lshl_add_u64 v[158:159], v[158:159], 0, s[72:73]
	s_waitcnt vmcnt(23)
	s_waitcnt lgkmcnt(5)
	v_mfma_f32_32x32x16_f16 v[2:17], v[114:117], v[106:109], v[2:17]
	s_waitcnt lgkmcnt(4)
	v_mfma_f32_32x32x16_f16 v[18:33], v[118:121], v[106:109], v[18:33]
	ds_read_b128 v[114:117], v162 offset:17600
	ds_read_b128 v[118:121], v162 offset:26304
	global_load_dwordx4 v[106:109], v[158:159], off
	v_lshl_add_u64 v[158:159], v[158:159], 0, s[72:73]
	s_waitcnt vmcnt(23)
	s_waitcnt lgkmcnt(5)
	v_mfma_f32_32x32x16_f16 v[2:17], v[122:125], v[142:145], v[2:17]
	s_waitcnt lgkmcnt(4)
	v_mfma_f32_32x32x16_f16 v[18:33], v[126:129], v[142:145], v[18:33]
	ds_read_b128 v[122:125], v162 offset:17632
	ds_read_b128 v[126:129], v162 offset:26336
	global_load_dwordx4 v[142:145], v[158:159], off
	v_lshl_add_u64 v[158:159], v[158:159], 0, s[72:73]
	s_waitcnt vmcnt(23)
	s_waitcnt lgkmcnt(5)
	v_mfma_f32_32x32x16_f16 v[2:17], v[130:133], v[146:149], v[2:17]
	s_waitcnt lgkmcnt(4)
	v_mfma_f32_32x32x16_f16 v[18:33], v[134:137], v[146:149], v[18:33]
	global_load_dwordx4 v[146:149], v[158:159], off
	v_lshl_add_u64 v[158:159], v[158:159], 0, s[72:73]
	s_waitcnt vmcnt(23)
	s_waitcnt lgkmcnt(3)
	v_mfma_f32_32x32x16_f16 v[2:17], v[114:117], v[150:153], v[2:17]
	s_waitcnt lgkmcnt(2)
	v_mfma_f32_32x32x16_f16 v[18:33], v[118:121], v[150:153], v[18:33]
	global_load_dwordx4 v[150:153], v[158:159], off
	v_lshl_add_u64 v[158:159], v[158:159], 0, s[72:73]
	s_waitcnt vmcnt(23)
	s_waitcnt lgkmcnt(1)
	v_mfma_f32_32x32x16_f16 v[2:17], v[122:125], v[154:157], v[2:17]
	s_waitcnt lgkmcnt(0)
	v_mfma_f32_32x32x16_f16 v[18:33], v[126:129], v[154:157], v[18:33]
	global_load_dwordx4 v[154:157], v[158:159], off
	v_lshl_add_u64 v[158:159], v[158:159], 0, s[72:73]
	s_waitcnt lgkmcnt(0)
	s_barrier
	ds_read_b128 v[114:117], v162 offset:34816
	ds_read_b128 v[118:121], v162 offset:43520
	ds_read_b128 v[122:125], v162 offset:34848
	ds_read_b128 v[126:129], v162 offset:43552
	ds_read_b128 v[130:133], v162 offset:34880
	ds_read_b128 v[134:137], v162 offset:43584
	s_waitcnt vmcnt(23)
	s_waitcnt lgkmcnt(5)
	v_mfma_f32_32x32x16_f16 v[2:17], v[114:117], v[110:113], v[2:17]
	s_waitcnt lgkmcnt(4)
	v_mfma_f32_32x32x16_f16 v[18:33], v[118:121], v[110:113], v[18:33]
	ds_read_b128 v[114:117], v162 offset:34912
	ds_read_b128 v[118:121], v162 offset:43616
	global_load_dwordx4 v[110:113], v[158:159], off
	v_lshl_add_u64 v[158:159], v[158:159], 0, s[72:73]
	s_waitcnt vmcnt(23)
	s_waitcnt lgkmcnt(5)
	v_mfma_f32_32x32x16_f16 v[2:17], v[122:125], v[90:93], v[2:17]
	s_waitcnt lgkmcnt(4)
	v_mfma_f32_32x32x16_f16 v[18:33], v[126:129], v[90:93], v[18:33]
	ds_read_b128 v[122:125], v162 offset:34944
	ds_read_b128 v[126:129], v162 offset:43648
	global_load_dwordx4 v[90:93], v[158:159], off
	v_lshl_add_u64 v[158:159], v[158:159], 0, s[72:73]
	s_waitcnt vmcnt(23)
	s_waitcnt lgkmcnt(5)
	v_mfma_f32_32x32x16_f16 v[2:17], v[130:133], v[86:89], v[2:17]
	s_waitcnt lgkmcnt(4)
	v_mfma_f32_32x32x16_f16 v[18:33], v[134:137], v[86:89], v[18:33]
	ds_read_b128 v[130:133], v162 offset:34976
	ds_read_b128 v[134:137], v162 offset:43680
	global_load_dwordx4 v[86:89], v[158:159], off
	v_lshl_add_u64 v[158:159], v[158:159], 0, s[72:73]
	s_waitcnt vmcnt(23)
	s_waitcnt lgkmcnt(5)
	v_mfma_f32_32x32x16_f16 v[2:17], v[114:117], v[82:85], v[2:17]
	s_waitcnt lgkmcnt(4)
	v_mfma_f32_32x32x16_f16 v[18:33], v[118:121], v[82:85], v[18:33]
	ds_read_b128 v[114:117], v162 offset:35008
	ds_read_b128 v[118:121], v162 offset:43712
	global_load_dwordx4 v[82:85], v[158:159], off
	v_lshl_add_u64 v[158:159], v[158:159], 0, s[72:73]
	s_waitcnt vmcnt(23)
	s_waitcnt lgkmcnt(5)
	v_mfma_f32_32x32x16_f16 v[2:17], v[122:125], v[78:81], v[2:17]
	s_waitcnt lgkmcnt(4)
	v_mfma_f32_32x32x16_f16 v[18:33], v[126:129], v[78:81], v[18:33]
	ds_read_b128 v[122:125], v162 offset:35040
	ds_read_b128 v[126:129], v162 offset:43744
	global_load_dwordx4 v[78:81], v[158:159], off
	v_lshl_add_u64 v[158:159], v[158:159], 0, s[72:73]
	s_waitcnt vmcnt(23)
	s_waitcnt lgkmcnt(5)
	v_mfma_f32_32x32x16_f16 v[2:17], v[130:133], v[74:77], v[2:17]
	s_waitcnt lgkmcnt(4)
	v_mfma_f32_32x32x16_f16 v[18:33], v[134:137], v[74:77], v[18:33]
	global_load_dwordx4 v[74:77], v[158:159], off
	v_lshl_add_u64 v[158:159], v[158:159], 0, s[72:73]
	s_waitcnt vmcnt(23)
	s_waitcnt lgkmcnt(3)
	v_mfma_f32_32x32x16_f16 v[2:17], v[114:117], v[70:73], v[2:17]
	s_waitcnt lgkmcnt(2)
	v_mfma_f32_32x32x16_f16 v[18:33], v[118:121], v[70:73], v[18:33]
	global_load_dwordx4 v[70:73], v[158:159], off
	v_lshl_add_u64 v[158:159], v[158:159], 0, s[72:73]
	s_waitcnt vmcnt(23)
	s_waitcnt lgkmcnt(1)
	v_mfma_f32_32x32x16_f16 v[2:17], v[122:125], v[66:69], v[2:17]
	s_waitcnt lgkmcnt(0)
	v_mfma_f32_32x32x16_f16 v[18:33], v[126:129], v[66:69], v[18:33]
	global_load_dwordx4 v[66:69], v[158:159], off
	v_lshl_add_u64 v[158:159], v[158:159], 0, s[72:73]
	s_waitcnt lgkmcnt(0)
	s_barrier
	ds_read_b128 v[114:117], v162 offset:52224
	ds_read_b128 v[118:121], v162 offset:60928
	ds_read_b128 v[122:125], v162 offset:52256
	ds_read_b128 v[126:129], v162 offset:60960
	ds_read_b128 v[130:133], v162 offset:52288
	ds_read_b128 v[134:137], v162 offset:60992
	s_waitcnt vmcnt(23)
	s_waitcnt lgkmcnt(5)
	v_mfma_f32_32x32x16_f16 v[2:17], v[114:117], v[62:65], v[2:17]
	s_waitcnt lgkmcnt(4)
	v_mfma_f32_32x32x16_f16 v[18:33], v[118:121], v[62:65], v[18:33]
	ds_read_b128 v[114:117], v162 offset:52320
	ds_read_b128 v[118:121], v162 offset:61024
	global_load_dwordx4 v[62:65], v[158:159], off
	v_lshl_add_u64 v[158:159], v[158:159], 0, s[72:73]
	s_waitcnt vmcnt(23)
	s_waitcnt lgkmcnt(5)
	v_mfma_f32_32x32x16_f16 v[2:17], v[122:125], v[58:61], v[2:17]
	s_waitcnt lgkmcnt(4)
	v_mfma_f32_32x32x16_f16 v[18:33], v[126:129], v[58:61], v[18:33]
	ds_read_b128 v[122:125], v162 offset:52352
	ds_read_b128 v[126:129], v162 offset:61056
	global_load_dwordx4 v[58:61], v[158:159], off
	v_lshl_add_u64 v[158:159], v[158:159], 0, s[72:73]
	s_waitcnt vmcnt(23)
	s_waitcnt lgkmcnt(5)
	v_mfma_f32_32x32x16_f16 v[2:17], v[130:133], v[54:57], v[2:17]
	s_waitcnt lgkmcnt(4)
	v_mfma_f32_32x32x16_f16 v[18:33], v[134:137], v[54:57], v[18:33]
	ds_read_b128 v[130:133], v162 offset:52384
	ds_read_b128 v[134:137], v162 offset:61088
	global_load_dwordx4 v[54:57], v[158:159], off
	v_lshl_add_u64 v[158:159], v[158:159], 0, s[72:73]
	s_waitcnt vmcnt(23)
	s_waitcnt lgkmcnt(5)
	v_mfma_f32_32x32x16_f16 v[2:17], v[114:117], v[50:53], v[2:17]
	s_waitcnt lgkmcnt(4)
	v_mfma_f32_32x32x16_f16 v[18:33], v[118:121], v[50:53], v[18:33]
	ds_read_b128 v[114:117], v162 offset:52416
	ds_read_b128 v[118:121], v162 offset:61120
	global_load_dwordx4 v[50:53], v[158:159], off
	v_lshl_add_u64 v[158:159], v[158:159], 0, s[72:73]
	s_waitcnt vmcnt(23)
	s_waitcnt lgkmcnt(5)
	v_mfma_f32_32x32x16_f16 v[2:17], v[122:125], v[46:49], v[2:17]
	s_waitcnt lgkmcnt(4)
	v_mfma_f32_32x32x16_f16 v[18:33], v[126:129], v[46:49], v[18:33]
	ds_read_b128 v[122:125], v162 offset:52448
	ds_read_b128 v[126:129], v162 offset:61152
	global_load_dwordx4 v[46:49], v[158:159], off
	v_lshl_add_u64 v[158:159], v[158:159], 0, s[72:73]
	s_waitcnt vmcnt(23)
	s_waitcnt lgkmcnt(5)
	v_mfma_f32_32x32x16_f16 v[2:17], v[130:133], v[42:45], v[2:17]
	s_waitcnt lgkmcnt(4)
	v_mfma_f32_32x32x16_f16 v[18:33], v[134:137], v[42:45], v[18:33]
	global_load_dwordx4 v[42:45], v[158:159], off
	v_lshl_add_u64 v[158:159], v[158:159], 0, s[72:73]
	s_waitcnt vmcnt(23)
	s_waitcnt lgkmcnt(3)
	v_mfma_f32_32x32x16_f16 v[2:17], v[114:117], v[38:41], v[2:17]
	s_waitcnt lgkmcnt(2)
	v_mfma_f32_32x32x16_f16 v[18:33], v[118:121], v[38:41], v[18:33]
	global_load_dwordx4 v[38:41], v[158:159], off
	v_lshl_add_u64 v[158:159], v[158:159], 0, s[72:73]
	s_waitcnt vmcnt(23)
	s_waitcnt lgkmcnt(1)
	v_mfma_f32_32x32x16_f16 v[2:17], v[122:125], v[34:37], v[2:17]
	s_waitcnt lgkmcnt(0)
	v_mfma_f32_32x32x16_f16 v[18:33], v[126:129], v[34:37], v[18:33]
	global_load_dwordx4 v[34:37], v[158:159], off
	v_lshl_add_u64 v[158:159], v[158:159], 0, s[72:73]
	s_waitcnt lgkmcnt(0)
	s_barrier
	ds_read_b128 v[114:117], v162 offset:0
	ds_read_b128 v[118:121], v162 offset:8704
	ds_read_b128 v[122:125], v162 offset:32
	ds_read_b128 v[126:129], v162 offset:8736
	ds_read_b128 v[130:133], v162 offset:64
	ds_read_b128 v[134:137], v162 offset:8768
	s_waitcnt vmcnt(23)
	s_waitcnt lgkmcnt(5)
	v_mfma_f32_32x32x16_f16 v[2:17], v[114:117], v[94:97], v[2:17]
	s_waitcnt lgkmcnt(4)
	v_mfma_f32_32x32x16_f16 v[18:33], v[118:121], v[94:97], v[18:33]
	ds_read_b128 v[114:117], v162 offset:96
	ds_read_b128 v[118:121], v162 offset:8800
	global_load_dwordx4 v[94:97], v[158:159], off
	v_lshl_add_u64 v[158:159], v[158:159], 0, s[72:73]
	s_waitcnt vmcnt(23)
	s_waitcnt lgkmcnt(5)
	v_mfma_f32_32x32x16_f16 v[2:17], v[122:125], v[98:101], v[2:17]
	s_waitcnt lgkmcnt(4)
	v_mfma_f32_32x32x16_f16 v[18:33], v[126:129], v[98:101], v[18:33]
	ds_read_b128 v[122:125], v162 offset:128
	ds_read_b128 v[126:129], v162 offset:8832
	global_load_dwordx4 v[98:101], v[158:159], off
	v_lshl_add_u64 v[158:159], v[158:159], 0, s[72:73]
	s_waitcnt vmcnt(23)
	s_waitcnt lgkmcnt(5)
	v_mfma_f32_32x32x16_f16 v[2:17], v[130:133], v[102:105], v[2:17]
	s_waitcnt lgkmcnt(4)
	v_mfma_f32_32x32x16_f16 v[18:33], v[134:137], v[102:105], v[18:33]
	ds_read_b128 v[130:133], v162 offset:160
	ds_read_b128 v[134:137], v162 offset:8864
	global_load_dwordx4 v[102:105], v[158:159], off
	v_lshl_add_u64 v[158:159], v[158:159], 0, s[72:73]
	s_waitcnt vmcnt(23)
	s_waitcnt lgkmcnt(5)
	v_mfma_f32_32x32x16_f16 v[2:17], v[114:117], v[106:109], v[2:17]
	s_waitcnt lgkmcnt(4)
	v_mfma_f32_32x32x16_f16 v[18:33], v[118:121], v[106:109], v[18:33]
	ds_read_b128 v[114:117], v162 offset:192
	ds_read_b128 v[118:121], v162 offset:8896
	global_load_dwordx4 v[106:109], v[158:159], off
	v_lshl_add_u64 v[158:159], v[158:159], 0, s[72:73]
	s_waitcnt vmcnt(23)
	s_waitcnt lgkmcnt(5)
	v_mfma_f32_32x32x16_f16 v[2:17], v[122:125], v[142:145], v[2:17]
	s_waitcnt lgkmcnt(4)
	v_mfma_f32_32x32x16_f16 v[18:33], v[126:129], v[142:145], v[18:33]
	ds_read_b128 v[122:125], v162 offset:224
	ds_read_b128 v[126:129], v162 offset:8928
	global_load_dwordx4 v[142:145], v[158:159], off
	v_lshl_add_u64 v[158:159], v[158:159], 0, s[72:73]
	s_waitcnt vmcnt(23)
	s_waitcnt lgkmcnt(5)
	v_mfma_f32_32x32x16_f16 v[2:17], v[130:133], v[146:149], v[2:17]
	s_waitcnt lgkmcnt(4)
	v_mfma_f32_32x32x16_f16 v[18:33], v[134:137], v[146:149], v[18:33]
	global_load_dwordx4 v[146:149], v[158:159], off
	v_lshl_add_u64 v[158:159], v[158:159], 0, s[72:73]
	s_waitcnt vmcnt(23)
	s_waitcnt lgkmcnt(3)
	v_mfma_f32_32x32x16_f16 v[2:17], v[114:117], v[150:153], v[2:17]
	s_waitcnt lgkmcnt(2)
	v_mfma_f32_32x32x16_f16 v[18:33], v[118:121], v[150:153], v[18:33]
	global_load_dwordx4 v[150:153], v[158:159], off
	v_lshl_add_u64 v[158:159], v[158:159], 0, s[72:73]
	s_waitcnt vmcnt(23)
	s_waitcnt lgkmcnt(1)
	v_mfma_f32_32x32x16_f16 v[2:17], v[122:125], v[154:157], v[2:17]
	s_waitcnt lgkmcnt(0)
	v_mfma_f32_32x32x16_f16 v[18:33], v[126:129], v[154:157], v[18:33]
	global_load_dwordx4 v[154:157], v[158:159], off
	v_lshl_add_u64 v[158:159], v[158:159], 0, s[72:73]
	s_waitcnt lgkmcnt(0)
	s_barrier
	ds_read_b128 v[114:117], v162 offset:17408
	ds_read_b128 v[118:121], v162 offset:26112
	ds_read_b128 v[122:125], v162 offset:17440
	ds_read_b128 v[126:129], v162 offset:26144
	ds_read_b128 v[130:133], v162 offset:17472
	ds_read_b128 v[134:137], v162 offset:26176
	s_waitcnt vmcnt(23)
	s_waitcnt lgkmcnt(5)
	v_mfma_f32_32x32x16_f16 v[2:17], v[114:117], v[110:113], v[2:17]
	s_waitcnt lgkmcnt(4)
	v_mfma_f32_32x32x16_f16 v[18:33], v[118:121], v[110:113], v[18:33]
	ds_read_b128 v[114:117], v162 offset:17504
	ds_read_b128 v[118:121], v162 offset:26208
	s_waitcnt vmcnt(22)
	s_waitcnt lgkmcnt(5)
	v_mfma_f32_32x32x16_f16 v[2:17], v[122:125], v[90:93], v[2:17]
	s_waitcnt lgkmcnt(4)
	v_mfma_f32_32x32x16_f16 v[18:33], v[126:129], v[90:93], v[18:33]
	ds_read_b128 v[122:125], v162 offset:17536
	ds_read_b128 v[126:129], v162 offset:26240
	s_waitcnt vmcnt(21)
	s_waitcnt lgkmcnt(5)
	v_mfma_f32_32x32x16_f16 v[2:17], v[130:133], v[86:89], v[2:17]
	s_waitcnt lgkmcnt(4)
	v_mfma_f32_32x32x16_f16 v[18:33], v[134:137], v[86:89], v[18:33]
	ds_read_b128 v[130:133], v162 offset:17568
	ds_read_b128 v[134:137], v162 offset:26272
	s_waitcnt vmcnt(20)
	s_waitcnt lgkmcnt(5)
	v_mfma_f32_32x32x16_f16 v[2:17], v[114:117], v[82:85], v[2:17]
	s_waitcnt lgkmcnt(4)
	v_mfma_f32_32x32x16_f16 v[18:33], v[118:121], v[82:85], v[18:33]
	ds_read_b128 v[114:117], v162 offset:17600
	ds_read_b128 v[118:121], v162 offset:26304
	s_waitcnt vmcnt(19)
	s_waitcnt lgkmcnt(5)
	v_mfma_f32_32x32x16_f16 v[2:17], v[122:125], v[78:81], v[2:17]
	s_waitcnt lgkmcnt(4)
	v_mfma_f32_32x32x16_f16 v[18:33], v[126:129], v[78:81], v[18:33]
	ds_read_b128 v[122:125], v162 offset:17632
	ds_read_b128 v[126:129], v162 offset:26336
	s_waitcnt vmcnt(18)
	s_waitcnt lgkmcnt(5)
	v_mfma_f32_32x32x16_f16 v[2:17], v[130:133], v[74:77], v[2:17]
	s_waitcnt lgkmcnt(4)
	v_mfma_f32_32x32x16_f16 v[18:33], v[134:137], v[74:77], v[18:33]
	s_waitcnt vmcnt(17)
	s_waitcnt lgkmcnt(3)
	v_mfma_f32_32x32x16_f16 v[2:17], v[114:117], v[70:73], v[2:17]
	s_waitcnt lgkmcnt(2)
	v_mfma_f32_32x32x16_f16 v[18:33], v[118:121], v[70:73], v[18:33]
	s_waitcnt vmcnt(16)
	s_waitcnt lgkmcnt(1)
	v_mfma_f32_32x32x16_f16 v[2:17], v[122:125], v[66:69], v[2:17]
	s_waitcnt lgkmcnt(0)
	v_mfma_f32_32x32x16_f16 v[18:33], v[126:129], v[66:69], v[18:33]
	s_waitcnt lgkmcnt(0)
	s_barrier
	ds_read_b128 v[114:117], v162 offset:34816
	ds_read_b128 v[118:121], v162 offset:43520
	ds_read_b128 v[122:125], v162 offset:34848
	ds_read_b128 v[126:129], v162 offset:43552
	ds_read_b128 v[130:133], v162 offset:34880
	ds_read_b128 v[134:137], v162 offset:43584
	s_waitcnt vmcnt(15)
	s_waitcnt lgkmcnt(5)
	v_mfma_f32_32x32x16_f16 v[2:17], v[114:117], v[62:65], v[2:17]
	s_waitcnt lgkmcnt(4)
	v_mfma_f32_32x32x16_f16 v[18:33], v[118:121], v[62:65], v[18:33]
	ds_read_b128 v[114:117], v162 offset:34912
	ds_read_b128 v[118:121], v162 offset:43616
	s_waitcnt vmcnt(14)
	s_waitcnt lgkmcnt(5)
	v_mfma_f32_32x32x16_f16 v[2:17], v[122:125], v[58:61], v[2:17]
	s_waitcnt lgkmcnt(4)
	v_mfma_f32_32x32x16_f16 v[18:33], v[126:129], v[58:61], v[18:33]
	ds_read_b128 v[122:125], v162 offset:34944
	ds_read_b128 v[126:129], v162 offset:43648
	s_waitcnt vmcnt(13)
	s_waitcnt lgkmcnt(5)
	v_mfma_f32_32x32x16_f16 v[2:17], v[130:133], v[54:57], v[2:17]
	s_waitcnt lgkmcnt(4)
	v_mfma_f32_32x32x16_f16 v[18:33], v[134:137], v[54:57], v[18:33]
	ds_read_b128 v[130:133], v162 offset:34976
	ds_read_b128 v[134:137], v162 offset:43680
	s_waitcnt vmcnt(12)
	s_waitcnt lgkmcnt(5)
	v_mfma_f32_32x32x16_f16 v[2:17], v[114:117], v[50:53], v[2:17]
	s_waitcnt lgkmcnt(4)
	v_mfma_f32_32x32x16_f16 v[18:33], v[118:121], v[50:53], v[18:33]
	ds_read_b128 v[114:117], v162 offset:35008
	ds_read_b128 v[118:121], v162 offset:43712
	s_waitcnt vmcnt(11)
	s_waitcnt lgkmcnt(5)
	v_mfma_f32_32x32x16_f16 v[2:17], v[122:125], v[46:49], v[2:17]
	s_waitcnt lgkmcnt(4)
	v_mfma_f32_32x32x16_f16 v[18:33], v[126:129], v[46:49], v[18:33]
	ds_read_b128 v[122:125], v162 offset:35040
	ds_read_b128 v[126:129], v162 offset:43744
	s_waitcnt vmcnt(10)
	s_waitcnt lgkmcnt(5)
	v_mfma_f32_32x32x16_f16 v[2:17], v[130:133], v[42:45], v[2:17]
	s_waitcnt lgkmcnt(4)
	v_mfma_f32_32x32x16_f16 v[18:33], v[134:137], v[42:45], v[18:33]
	s_waitcnt vmcnt(9)
	s_waitcnt lgkmcnt(3)
	v_mfma_f32_32x32x16_f16 v[2:17], v[114:117], v[38:41], v[2:17]
	s_waitcnt lgkmcnt(2)
	v_mfma_f32_32x32x16_f16 v[18:33], v[118:121], v[38:41], v[18:33]
	s_waitcnt vmcnt(8)
	s_waitcnt lgkmcnt(1)
	v_mfma_f32_32x32x16_f16 v[2:17], v[122:125], v[34:37], v[2:17]
	s_waitcnt lgkmcnt(0)
	v_mfma_f32_32x32x16_f16 v[18:33], v[126:129], v[34:37], v[18:33]
	s_waitcnt lgkmcnt(0)
	s_barrier
	ds_read_b128 v[114:117], v162 offset:52224
	ds_read_b128 v[118:121], v162 offset:60928
	ds_read_b128 v[122:125], v162 offset:52256
	ds_read_b128 v[126:129], v162 offset:60960
	ds_read_b128 v[130:133], v162 offset:52288
	ds_read_b128 v[134:137], v162 offset:60992
	s_waitcnt vmcnt(7)
	s_waitcnt lgkmcnt(5)
	v_mfma_f32_32x32x16_f16 v[2:17], v[114:117], v[94:97], v[2:17]
	s_waitcnt lgkmcnt(4)
	v_mfma_f32_32x32x16_f16 v[18:33], v[118:121], v[94:97], v[18:33]
	ds_read_b128 v[114:117], v162 offset:52320
	ds_read_b128 v[118:121], v162 offset:61024
	s_waitcnt vmcnt(6)
	s_waitcnt lgkmcnt(5)
	v_mfma_f32_32x32x16_f16 v[2:17], v[122:125], v[98:101], v[2:17]
	s_waitcnt lgkmcnt(4)
	v_mfma_f32_32x32x16_f16 v[18:33], v[126:129], v[98:101], v[18:33]
	ds_read_b128 v[122:125], v162 offset:52352
	ds_read_b128 v[126:129], v162 offset:61056
	s_waitcnt vmcnt(5)
	s_waitcnt lgkmcnt(5)
	v_mfma_f32_32x32x16_f16 v[2:17], v[130:133], v[102:105], v[2:17]
	s_waitcnt lgkmcnt(4)
	v_mfma_f32_32x32x16_f16 v[18:33], v[134:137], v[102:105], v[18:33]
	ds_read_b128 v[130:133], v162 offset:52384
	ds_read_b128 v[134:137], v162 offset:61088
	s_waitcnt vmcnt(4)
	s_waitcnt lgkmcnt(5)
	v_mfma_f32_32x32x16_f16 v[2:17], v[114:117], v[106:109], v[2:17]
	s_waitcnt lgkmcnt(4)
	v_mfma_f32_32x32x16_f16 v[18:33], v[118:121], v[106:109], v[18:33]
	ds_read_b128 v[114:117], v162 offset:52416
	ds_read_b128 v[118:121], v162 offset:61120
	s_waitcnt vmcnt(3)
	s_waitcnt lgkmcnt(5)
	v_mfma_f32_32x32x16_f16 v[2:17], v[122:125], v[142:145], v[2:17]
	s_waitcnt lgkmcnt(4)
	v_mfma_f32_32x32x16_f16 v[18:33], v[126:129], v[142:145], v[18:33]
	ds_read_b128 v[122:125], v162 offset:52448
	ds_read_b128 v[126:129], v162 offset:61152
	s_waitcnt vmcnt(2)
	s_waitcnt lgkmcnt(5)
	v_mfma_f32_32x32x16_f16 v[2:17], v[130:133], v[146:149], v[2:17]
	s_waitcnt lgkmcnt(4)
	v_mfma_f32_32x32x16_f16 v[18:33], v[134:137], v[146:149], v[18:33]
	s_waitcnt vmcnt(1)
	s_waitcnt lgkmcnt(3)
	v_mfma_f32_32x32x16_f16 v[2:17], v[114:117], v[150:153], v[2:17]
	s_waitcnt lgkmcnt(2)
	v_mfma_f32_32x32x16_f16 v[18:33], v[118:121], v[150:153], v[18:33]
	s_waitcnt vmcnt(0)
	s_waitcnt lgkmcnt(1)
	v_mfma_f32_32x32x16_f16 v[2:17], v[122:125], v[154:157], v[2:17]
	s_waitcnt lgkmcnt(0)
	v_mfma_f32_32x32x16_f16 v[18:33], v[126:129], v[154:157], v[18:33]
	s_waitcnt lgkmcnt(0)
	s_barrier
	s_mov_b32 s2, 0x3d800000
	v_mul_u32_u24_e32 v1, 0x420, v1
	v_or_b32_e32 v34, v161, v160
	v_lshlrev_b32_e32 v34, 1, v34
	v_lshl_add_u32 v1, v1, 1, v34
	s_nop 7
	s_nop 7
	v_fma_mixlo_f16 v2, v2, s2, 0
	ds_write_b16 v1, v2
	v_fma_mixlo_f16 v2, v18, s2, 0
	ds_write_b16 v1, v2 offset:16896
	v_fma_mixlo_f16 v2, v3, s2, 0
	ds_write_b16 v1, v2 offset:528
	v_fma_mixlo_f16 v2, v19, s2, 0
	ds_write_b16 v1, v2 offset:17424
	v_fma_mixlo_f16 v2, v4, s2, 0
	ds_write_b16 v1, v2 offset:1056
	v_fma_mixlo_f16 v2, v20, s2, 0
	ds_write_b16 v1, v2 offset:17952
	v_fma_mixlo_f16 v2, v5, s2, 0
	ds_write_b16 v1, v2 offset:1584
	v_fma_mixlo_f16 v2, v21, s2, 0
	ds_write_b16 v1, v2 offset:18480
	v_fma_mixlo_f16 v2, v6, s2, 0
	ds_write_b16 v1, v2 offset:4224
	v_fma_mixlo_f16 v2, v22, s2, 0
	ds_write_b16 v1, v2 offset:21120
	v_fma_mixlo_f16 v2, v7, s2, 0
	ds_write_b16 v1, v2 offset:4752
	v_fma_mixlo_f16 v2, v23, s2, 0
	ds_write_b16 v1, v2 offset:21648
	v_fma_mixlo_f16 v2, v8, s2, 0
	ds_write_b16 v1, v2 offset:5280
	v_fma_mixlo_f16 v2, v24, s2, 0
	ds_write_b16 v1, v2 offset:22176
	v_fma_mixlo_f16 v2, v9, s2, 0
	ds_write_b16 v1, v2 offset:5808
	v_fma_mixlo_f16 v2, v25, s2, 0
	ds_write_b16 v1, v2 offset:22704
	v_fma_mixlo_f16 v2, v10, s2, 0
	ds_write_b16 v1, v2 offset:8448
	v_fma_mixlo_f16 v2, v26, s2, 0
	ds_write_b16 v1, v2 offset:25344
	v_fma_mixlo_f16 v2, v11, s2, 0
	ds_write_b16 v1, v2 offset:8976
	v_fma_mixlo_f16 v2, v27, s2, 0
	ds_write_b16 v1, v2 offset:25872
	v_fma_mixlo_f16 v2, v12, s2, 0
	ds_write_b16 v1, v2 offset:9504
	v_fma_mixlo_f16 v2, v28, s2, 0
	ds_write_b16 v1, v2 offset:26400
	v_fma_mixlo_f16 v2, v13, s2, 0
	ds_write_b16 v1, v2 offset:10032
	v_fma_mixlo_f16 v2, v29, s2, 0
	ds_write_b16 v1, v2 offset:26928
	v_fma_mixlo_f16 v2, v14, s2, 0
	ds_write_b16 v1, v2 offset:12672
	v_fma_mixlo_f16 v2, v30, s2, 0
	ds_write_b16 v1, v2 offset:29568
	v_fma_mixlo_f16 v2, v15, s2, 0
	ds_write_b16 v1, v2 offset:13200
	v_fma_mixlo_f16 v2, v31, s2, 0
	ds_write_b16 v1, v2 offset:30096
	v_fma_mixlo_f16 v2, v16, s2, 0
	ds_write_b16 v1, v2 offset:13728
	v_fma_mixlo_f16 v2, v32, s2, 0
	ds_write_b16 v1, v2 offset:30624
	v_fma_mixlo_f16 v2, v17, s2, 0
	ds_write_b16 v1, v2 offset:14256
	v_fma_mixlo_f16 v2, v33, s2, 0
	ds_write_b16 v1, v2 offset:31152
	v_lshrrev_b32_e32 v1, 3, v0
	v_lshlrev_b32_e32 v0, 4, v0
	v_and_b32_e32 v4, 0x70, v0
	s_movk_i32 s2, 0x210
	v_mad_u32_u24 v12, v1, s2, v4
	s_ashr_i32 s2, s8, 31
	s_waitcnt lgkmcnt(0)
	s_barrier
	v_or_b32_e32 v6, s8, v1
	v_mov_b32_e32 v7, s2
	v_mov_b32_e32 v5, 0
	ds_read_b128 v[0:3], v12
	v_lshl_add_u64 v[4:5], s[16:17], 0, v[4:5]
	v_lshlrev_b64 v[6:7], 7, v[6:7]
	v_lshl_add_u64 v[8:9], v[4:5], 0, v[6:7]
	ds_read_b128 v[4:7], v12 offset:128
	s_mov_b32 s2, 0x200000
	s_waitcnt lgkmcnt(1)
	global_store_dwordx4 v[8:9], v[0:3], off
	s_nop 1
	v_add_co_u32_e32 v0, vcc, s2, v8
	s_nop 1
	v_addc_co_u32_e32 v1, vcc, 0, v9, vcc
	s_waitcnt lgkmcnt(0)
	global_store_dwordx4 v[0:1], v[4:7], off
	ds_read_b128 v[0:3], v12 offset:256
	ds_read_b128 v[4:7], v12 offset:384
	v_add_co_u32_e32 v10, vcc, 0x400000, v8
	s_nop 1
	v_addc_co_u32_e32 v11, vcc, 0, v9, vcc
	s_waitcnt lgkmcnt(1)
	global_store_dwordx4 v[10:11], v[0:3], off
	s_nop 1
	v_add_co_u32_e32 v0, vcc, 0x600000, v8
	s_nop 1
	v_addc_co_u32_e32 v1, vcc, 0, v9, vcc
	s_waitcnt lgkmcnt(0)
	global_store_dwordx4 v[0:1], v[4:7], off
	s_andn2_saveexec_b64 s[0:1], s[0:1]
	s_cbranch_execz .LBB1_234
